# FFN-up epilogue: the remaining dead register-sourced initialisations before full-mask row_ror DPP moves also replaced by s_nop
# baseline (speedup 1.0000x reference)
.LBB0_1669:
	s_or_b64 exec, exec, s[34:35]
	v_or_b32_e32 v103, 0xffffffe0, v102
	v_add_u32_e32 v102, s60, v103
	v_lshl_add_u32 v195, v144, 2, s75
	s_and_b64 s[40:41], s[18:19], vcc
	v_mov_b32_e32 v108, 0
	v_lshl_add_u32 v171, v102, 9, v195
	v_mov_b32_e32 v144, 0
	v_mov_b32_e32 v145, 0
	v_mov_b32_e32 v146, 0
	v_mov_b32_e32 v147, 0
	s_and_saveexec_b64 s[34:35], s[40:41]
	ds_read_b128 v[144:147], v171
	s_or_b64 exec, exec, s[34:35]
	v_mov_b32_e32 v109, 0
	v_mov_b32_e32 v110, 0
	v_mov_b32_e32 v111, 0
	s_and_saveexec_b64 s[34:35], s[40:41]
	ds_read_b128 v[108:111], v171 offset:512
	s_or_b64 exec, exec, s[34:35]
	s_waitcnt lgkmcnt(0)
	v_pk_mul_f32 v[222:223], v[128:129], v[140:141]
	v_pk_mul_f32 v[224:225], v[128:129], v[136:137]
	v_pk_mul_f32 v[226:227], v[128:129], v[132:133]
	v_pk_mul_f32 v[124:125], v[112:113], v[124:125]
	v_pk_mul_f32 v[128:129], v[114:115], v[122:123]
	v_pk_mul_f32 v[120:121], v[112:113], v[120:121]
	v_pk_mul_f32 v[122:123], v[112:113], v[116:117]
	v_cvt_f32_i32_e32 v113, v22
	v_cvt_f32_i32_e32 v112, v46
	s_nop 0
	s_nop 0
	v_pk_mul_f32 v[142:143], v[130:131], v[142:143]
	v_pk_mul_f32 v[220:221], v[130:131], v[138:139]
	v_pk_mul_f32 v[140:141], v[130:131], v[134:135]
	v_pk_mul_f32 v[130:131], v[114:115], v[118:119]
	s_nop 0
	v_mov_b32_dpp v116, v144 row_ror:2 row_mask:0xf bank_mask:0xf
	s_nop 0
	v_mov_b32_dpp v117, v108 row_ror:2 row_mask:0xf bank_mask:0xf
	s_waitcnt vmcnt(0)
	v_mov_b32_e32 v250, s26
	v_min_u32_e32 v250, 0x55, v250
	v_mul_u32_u24_e32 v250, v250, v231
	v_mov_b32_e32 v251, 0
	v_lshl_add_u64 v[248:249], v[250:251], 0, v[252:253]
	global_load_dwordx4 v[248:251], v[248:249], off
	v_mov_b32_e32 v246, s28
	v_min_u32_e32 v246, 64, v246
	v_lshl_add_u32 v246, v246, 8, s55
	v_and_or_b32 v246, v166, 15, v246
	v_lshlrev_b32_e32 v246, 2, v246
	global_load_dword v240, v246, s[20:21]
	global_load_dword v241, v246, s[20:21] offset:64
	global_load_dword v242, v246, s[20:21] offset:128
	global_load_dword v243, v246, s[20:21] offset:192
	global_load_dword v244, v246, s[20:21] offset:512
	global_load_dword v245, v246, s[20:21] offset:576
	global_load_dword v247, v246, s[20:21] offset:704
	global_load_dword v246, v246, s[20:21] offset:640
	v_pk_mul_f32 v[236:237], v[172:173], v[112:113] op_sel_hi:[0,1]
	v_pk_mul_f32 v[126:127], v[114:115], v[126:127]
	v_mov_b32_dpp v118, v144 row_ror:1 row_mask:0xf bank_mask:0xf
	s_nop 0
	s_nop 0
	s_nop 0
	s_nop 0
	v_mov_b32_dpp v119, v108 row_ror:1 row_mask:0xf bank_mask:0xf
	v_mov_b32_dpp v116, v236 row_shr:2 row_mask:0xf bank_mask:0xf
	v_mov_b32_dpp v117, v237 row_shr:2 row_mask:0xf bank_mask:0xf
	v_mov_b32_e32 v112, v124
	v_mov_b32_e32 v113, v222
	v_mov_b32_e32 v114, v104
	v_mov_b32_e32 v115, v98
	v_mov_b32_dpp v136, v146 row_ror:1 row_mask:0xf bank_mask:0xf
	v_mov_b32_dpp v144, v146 row_ror:2 row_mask:0xf bank_mask:0xf
	v_mov_b32_dpp v232, v147 row_ror:1 row_mask:0xf bank_mask:0xf
	v_mov_b32_dpp v234, v147 row_ror:2 row_mask:0xf bank_mask:0xf
	v_mov_b32_dpp v118, v236 row_shr:1 row_mask:0xf bank_mask:0xf
	v_mov_b32_dpp v119, v237 row_shr:1 row_mask:0xf bank_mask:0xf
	v_pk_fma_f32 v[146:147], v[112:113], v[116:117], v[114:115]
	v_mov_b32_e32 v116, v120
	v_mov_b32_e32 v117, v224
	v_pk_fma_f32 v[146:147], v[116:117], v[118:119], v[146:147]
	v_mov_b32_e32 v118, v122
	v_mov_b32_e32 v119, v226
	v_pk_fma_f32 v[238:239], v[236:237], v[118:119], v[146:147]
	v_cvt_f32_i32_e32 v147, v23
	v_cvt_f32_i32_e32 v146, v47
	s_nop 0
	s_nop 0
	s_nop 0
	v_mov_b32_dpp v134, v145 row_ror:2 row_mask:0xf bank_mask:0xf
	v_mov_b32_dpp v133, v109 row_ror:1 row_mask:0xf bank_mask:0xf
	v_mov_b32_dpp v135, v109 row_ror:2 row_mask:0xf bank_mask:0xf
	v_pk_mul_f32 v[108:109], v[172:173], v[146:147] op_sel_hi:[0,1]
	s_nop 0
	v_mov_b32_e32 v222, v125
	v_mov_b32_dpp v134, v108 row_shr:2 row_mask:0xf bank_mask:0xf
	v_mov_b32_dpp v135, v109 row_shr:2 row_mask:0xf bank_mask:0xf
	v_mov_b32_e32 v98, v105
	v_mov_b32_dpp v132, v145 row_ror:1 row_mask:0xf bank_mask:0xf
	v_pk_fma_f32 v[104:105], v[222:223], v[134:135], v[98:99]
	v_mov_b32_e32 v224, v121
	v_cvt_f32_i32_e32 v121, v24
	v_cvt_f32_i32_e32 v120, v48
	v_cvt_f32_i32_e32 v135, v25
	v_cvt_f32_i32_e32 v134, v49
	v_mov_b32_dpp v132, v108 row_shr:1 row_mask:0xf bank_mask:0xf
	v_mov_b32_dpp v133, v109 row_shr:1 row_mask:0xf bank_mask:0xf
	v_pk_fma_f32 v[104:105], v[224:225], v[132:133], v[104:105]
	v_mov_b32_e32 v226, v123
	v_pk_fma_f32 v[104:105], v[108:109], v[226:227], v[104:105]
	s_nop 0
	s_nop 0
	s_nop 0
	s_nop 0
	v_mov_b32_dpp v137, v110 row_ror:1 row_mask:0xf bank_mask:0xf
	v_mov_b32_dpp v145, v110 row_ror:2 row_mask:0xf bank_mask:0xf
	v_pk_mul_f32 v[132:133], v[172:173], v[120:121] op_sel_hi:[0,1]
	v_mov_b32_e32 v121, v142
	v_mov_b32_dpp v233, v111 row_ror:1 row_mask:0xf bank_mask:0xf
	v_mov_b32_dpp v235, v111 row_ror:2 row_mask:0xf bank_mask:0xf
	v_pk_mul_f32 v[110:111], v[172:173], v[134:135] op_sel_hi:[0,1]
	v_mov_b32_e32 v142, v127
	v_mul_f32_e32 v127, 0xbfb8aa3b, v104
	v_mov_b32_dpp v144, v132 row_shr:2 row_mask:0xf bank_mask:0xf
	v_mov_b32_dpp v145, v133 row_shr:2 row_mask:0xf bank_mask:0xf
	v_mov_b32_e32 v120, v126
	v_mov_b32_e32 v122, v106
	v_mov_b32_e32 v123, v100
	v_mov_b32_dpp v234, v110 row_shr:2 row_mask:0xf bank_mask:0xf
	v_mov_b32_dpp v235, v111 row_shr:2 row_mask:0xf bank_mask:0xf
	v_mov_b32_e32 v100, v107
	v_exp_f32_e32 v127, v127
	v_mov_b32_dpp v136, v132 row_shr:1 row_mask:0xf bank_mask:0xf
	v_mov_b32_dpp v137, v133 row_shr:1 row_mask:0xf bank_mask:0xf
	v_pk_fma_f32 v[124:125], v[120:121], v[144:145], v[122:123]
	v_mov_b32_e32 v144, v128
	v_mov_b32_e32 v145, v220
	v_mov_b32_dpp v232, v110 row_shr:1 row_mask:0xf bank_mask:0xf
	v_mov_b32_dpp v233, v111 row_shr:1 row_mask:0xf bank_mask:0xf
	v_pk_fma_f32 v[106:107], v[142:143], v[234:235], v[100:101]
	v_mov_b32_e32 v220, v129
	v_pk_fma_f32 v[124:125], v[144:145], v[136:137], v[124:125]
	v_mov_b32_e32 v146, v130
	v_mov_b32_e32 v147, v140
	v_pk_fma_f32 v[106:107], v[220:221], v[232:233], v[106:107]
	v_mov_b32_e32 v140, v131
	v_pk_fma_f32 v[124:125], v[132:133], v[146:147], v[124:125]
	v_pk_fma_f32 v[106:107], v[110:111], v[140:141], v[106:107]
	v_add_f32_e32 v127, 1.0, v127
	v_mul_f32_e32 v128, 0xbfb8aa3b, v124
	v_mul_f32_e32 v129, 0xbfb8aa3b, v106
	v_mul_f32_e32 v126, 0xbfb8aa3b, v238
	v_rcp_f32_e32 v127, v127
	v_exp_f32_e32 v128, v128
	v_exp_f32_e32 v129, v129
	v_exp_f32_e32 v126, v126
	v_mul_f32_e32 v104, v104, v127
	v_add_f32_e32 v127, 1.0, v128
	v_add_f32_e32 v128, 1.0, v129
	v_add_f32_e32 v126, 1.0, v126
	v_rcp_f32_e32 v127, v127
	v_rcp_f32_e32 v128, v128
	v_rcp_f32_e32 v126, v126
	v_cvt_f32_i32_e32 v137, v18
	v_cvt_f32_i32_e32 v136, v42
	v_mul_f32_e32 v104, v104, v105
	v_mul_f32_e32 v105, v124, v127
	v_mul_f32_e32 v106, v106, v128
	v_lshl_add_u64 v[138:139], v[156:157], 1, s[8:9]
	v_mul_f32_e32 v126, v238, v126
	v_mul_f32_e32 v105, v105, v125
	v_mul_f32_e32 v106, v106, v107
	v_mul_f32_e32 v126, v126, v239
	v_cvt_pk_bf16_f32 v104, v126, v104
	v_cvt_pk_bf16_f32 v105, v105, v106
	v_mad_u64_u32 v[124:125], s[34:35], v169, s72, v[138:139]
	s_nop 0
	s_nop 0
	global_store_dwordx2 v[124:125], v[104:105], off
	s_nop 0
	v_mov_b32_dpp v106, v236 row_ror:2 row_mask:0xf bank_mask:0xf
	s_nop 0
	v_mov_b32_dpp v107, v237 row_ror:2 row_mask:0xf bank_mask:0xf
	v_pk_mul_f32 v[136:137], v[170:171], v[136:137] op_sel_hi:[0,1]
	v_mov_b32_dpp v104, v236 row_ror:1 row_mask:0xf bank_mask:0xf
	v_mov_b32_dpp v105, v237 row_ror:1 row_mask:0xf bank_mask:0xf
	v_mov_b32_dpp v106, v136 row_shr:2 row_mask:0xf bank_mask:0xf
	v_mov_b32_dpp v107, v137 row_shr:2 row_mask:0xf bank_mask:0xf
	v_mov_b32_dpp v104, v136 row_shr:1 row_mask:0xf bank_mask:0xf
	v_mov_b32_dpp v105, v137 row_shr:1 row_mask:0xf bank_mask:0xf
	v_pk_fma_f32 v[106:107], v[112:113], v[106:107], v[114:115]
	s_nop 0
	v_pk_fma_f32 v[104:105], v[116:117], v[104:105], v[106:107]
	v_cvt_f32_i32_e32 v107, v19
	v_cvt_f32_i32_e32 v106, v43
	s_nop 0
	s_nop 0
	v_mov_b32_dpp v128, v108 row_ror:2 row_mask:0xf bank_mask:0xf
	s_nop 0
	v_mov_b32_dpp v129, v109 row_ror:2 row_mask:0xf bank_mask:0xf
	v_pk_mul_f32 v[106:107], v[170:171], v[106:107] op_sel_hi:[0,1]
	v_mov_b32_dpp v126, v108 row_ror:1 row_mask:0xf bank_mask:0xf
	v_mov_b32_dpp v127, v109 row_ror:1 row_mask:0xf bank_mask:0xf
	v_mov_b32_dpp v128, v106 row_shr:2 row_mask:0xf bank_mask:0xf
	v_mov_b32_dpp v129, v107 row_shr:2 row_mask:0xf bank_mask:0xf
	v_mov_b32_dpp v126, v106 row_shr:1 row_mask:0xf bank_mask:0xf
	v_mov_b32_dpp v127, v107 row_shr:1 row_mask:0xf bank_mask:0xf
	v_pk_fma_f32 v[128:129], v[222:223], v[128:129], v[98:99]
	s_nop 0
	v_pk_fma_f32 v[126:127], v[224:225], v[126:127], v[128:129]
	v_cvt_f32_i32_e32 v129, v20
	v_cvt_f32_i32_e32 v128, v44
	s_nop 0
	s_nop 0
	v_mov_b32_dpp v130, v132 row_ror:2 row_mask:0xf bank_mask:0xf
	s_nop 0
	v_mov_b32_dpp v131, v133 row_ror:2 row_mask:0xf bank_mask:0xf
	v_pk_mul_f32 v[128:129], v[170:171], v[128:129] op_sel_hi:[0,1]
	v_mov_b32_dpp v108, v132 row_ror:1 row_mask:0xf bank_mask:0xf
	v_mov_b32_dpp v109, v133 row_ror:1 row_mask:0xf bank_mask:0xf
	v_mov_b32_dpp v130, v128 row_shr:2 row_mask:0xf bank_mask:0xf
	v_mov_b32_dpp v131, v129 row_shr:2 row_mask:0xf bank_mask:0xf
	v_mov_b32_dpp v108, v128 row_shr:1 row_mask:0xf bank_mask:0xf
	v_mov_b32_dpp v109, v129 row_shr:1 row_mask:0xf bank_mask:0xf
	v_pk_fma_f32 v[130:131], v[120:121], v[130:131], v[122:123]
	s_nop 0
	v_pk_fma_f32 v[108:109], v[144:145], v[108:109], v[130:131]
	v_cvt_f32_i32_e32 v131, v21
	v_cvt_f32_i32_e32 v130, v45
	s_nop 0
	v_pk_fma_f32 v[104:105], v[136:137], v[118:119], v[104:105]
	s_nop 0
	s_nop 0
	v_mov_b32_dpp v132, v110 row_ror:1 row_mask:0xf bank_mask:0xf
	v_mov_b32_dpp v134, v110 row_ror:2 row_mask:0xf bank_mask:0xf
	v_mov_b32_dpp v133, v111 row_ror:1 row_mask:0xf bank_mask:0xf
	v_mov_b32_dpp v135, v111 row_ror:2 row_mask:0xf bank_mask:0xf
	v_pk_mul_f32 v[110:111], v[170:171], v[130:131] op_sel_hi:[0,1]
	v_mul_f32_e32 v130, 0xbfb8aa3b, v104
	v_exp_f32_e32 v207, v130
	v_mov_b32_dpp v134, v110 row_shr:2 row_mask:0xf bank_mask:0xf
	v_mov_b32_dpp v135, v111 row_shr:2 row_mask:0xf bank_mask:0xf
	v_mov_b32_dpp v132, v110 row_shr:1 row_mask:0xf bank_mask:0xf
	v_mov_b32_dpp v133, v111 row_shr:1 row_mask:0xf bank_mask:0xf
	v_pk_fma_f32 v[130:131], v[142:143], v[134:135], v[100:101]
	v_pk_fma_f32 v[126:127], v[106:107], v[226:227], v[126:127]
	v_pk_fma_f32 v[130:131], v[220:221], v[132:133], v[130:131]
	v_add_f32_e32 v132, 1.0, v207
	v_rcp_f32_e32 v132, v132
	v_mul_f32_e32 v133, 0xbfb8aa3b, v126
	v_exp_f32_e32 v133, v133
	v_pk_fma_f32 v[108:109], v[128:129], v[146:147], v[108:109]
	v_mul_f32_e32 v104, v104, v132
	v_pk_fma_f32 v[130:131], v[110:111], v[140:141], v[130:131]
	v_mul_f32_e32 v104, v104, v105
	v_add_f32_e32 v105, 1.0, v133
	v_mul_f32_e32 v132, 0xbfb8aa3b, v108
	v_rcp_f32_e32 v105, v105
	v_exp_f32_e32 v132, v132
	v_mul_f32_e32 v133, 0xbfb8aa3b, v130
	v_exp_f32_e32 v133, v133
	v_mul_f32_e32 v105, v126, v105
	v_add_f32_e32 v126, 1.0, v132
	v_rcp_f32_e32 v126, v126
	v_add_f32_e32 v132, 1.0, v133
	v_rcp_f32_e32 v132, v132
	v_cvt_f32_i32_e32 v233, v14
	v_mul_f32_e32 v108, v108, v126
	v_cvt_f32_i32_e32 v232, v38
	v_mul_f32_e32 v105, v105, v127
	v_mul_f32_e32 v108, v108, v109
	v_mul_f32_e32 v109, v130, v132
	v_mul_f32_e32 v109, v109, v131
	v_cvt_pk_bf16_f32 v104, v104, v105
	v_cvt_pk_bf16_f32 v105, v108, v109
	v_add_u32_e32 v108, 16, v169
	v_mad_u64_u32 v[126:127], s[34:35], v108, s72, v[138:139]
	s_nop 0
	s_nop 0
	global_store_dwordx2 v[126:127], v[104:105], off
	s_nop 0
	v_mov_b32_dpp v108, v136 row_ror:2 row_mask:0xf bank_mask:0xf
	s_nop 0
	v_mov_b32_dpp v109, v137 row_ror:2 row_mask:0xf bank_mask:0xf
	v_pk_mul_f32 v[232:233], v[168:169], v[232:233] op_sel_hi:[0,1]
	v_mov_b32_dpp v104, v136 row_ror:1 row_mask:0xf bank_mask:0xf
	v_mov_b32_dpp v105, v137 row_ror:1 row_mask:0xf bank_mask:0xf
	v_mov_b32_dpp v108, v232 row_shr:2 row_mask:0xf bank_mask:0xf
	v_mov_b32_dpp v109, v233 row_shr:2 row_mask:0xf bank_mask:0xf
	v_mov_b32_dpp v104, v232 row_shr:1 row_mask:0xf bank_mask:0xf
	v_mov_b32_dpp v105, v233 row_shr:1 row_mask:0xf bank_mask:0xf
	v_pk_fma_f32 v[108:109], v[112:113], v[108:109], v[114:115]
	s_nop 0
	v_pk_fma_f32 v[104:105], v[116:117], v[104:105], v[108:109]
	v_cvt_f32_i32_e32 v109, v15
	v_cvt_f32_i32_e32 v108, v39
	s_nop 0
	s_nop 0
	v_mov_b32_dpp v132, v106 row_ror:2 row_mask:0xf bank_mask:0xf
	s_nop 0
	v_mov_b32_dpp v133, v107 row_ror:2 row_mask:0xf bank_mask:0xf
	v_pk_mul_f32 v[108:109], v[168:169], v[108:109] op_sel_hi:[0,1]
	v_mov_b32_dpp v130, v106 row_ror:1 row_mask:0xf bank_mask:0xf
	v_mov_b32_dpp v131, v107 row_ror:1 row_mask:0xf bank_mask:0xf
	v_mov_b32_dpp v132, v108 row_shr:2 row_mask:0xf bank_mask:0xf
	v_mov_b32_dpp v133, v109 row_shr:2 row_mask:0xf bank_mask:0xf
	v_mov_b32_dpp v130, v108 row_shr:1 row_mask:0xf bank_mask:0xf
	v_mov_b32_dpp v131, v109 row_shr:1 row_mask:0xf bank_mask:0xf
	v_pk_fma_f32 v[132:133], v[222:223], v[132:133], v[98:99]
	s_nop 0
	v_pk_fma_f32 v[130:131], v[224:225], v[130:131], v[132:133]
	v_cvt_f32_i32_e32 v133, v16
	v_cvt_f32_i32_e32 v132, v40
	s_nop 0
	s_nop 0
	v_mov_b32_dpp v134, v128 row_ror:2 row_mask:0xf bank_mask:0xf
	s_nop 0
	v_mov_b32_dpp v135, v129 row_ror:2 row_mask:0xf bank_mask:0xf
	v_pk_mul_f32 v[132:133], v[168:169], v[132:133] op_sel_hi:[0,1]
	v_mov_b32_dpp v106, v128 row_ror:1 row_mask:0xf bank_mask:0xf
	v_mov_b32_dpp v107, v129 row_ror:1 row_mask:0xf bank_mask:0xf
	v_mov_b32_dpp v134, v132 row_shr:2 row_mask:0xf bank_mask:0xf
	v_mov_b32_dpp v135, v133 row_shr:2 row_mask:0xf bank_mask:0xf
	v_mov_b32_dpp v106, v132 row_shr:1 row_mask:0xf bank_mask:0xf
	v_mov_b32_dpp v107, v133 row_shr:1 row_mask:0xf bank_mask:0xf
	v_pk_fma_f32 v[134:135], v[120:121], v[134:135], v[122:123]
	s_nop 0
	v_pk_fma_f32 v[106:107], v[144:145], v[106:107], v[134:135]
	v_cvt_f32_i32_e32 v135, v17
	v_cvt_f32_i32_e32 v134, v41
	s_nop 0
	v_pk_fma_f32 v[104:105], v[232:233], v[118:119], v[104:105]
	s_nop 0
	s_nop 0
	v_mov_b32_dpp v128, v110 row_ror:1 row_mask:0xf bank_mask:0xf
	v_mov_b32_dpp v136, v110 row_ror:2 row_mask:0xf bank_mask:0xf
	v_mov_b32_dpp v129, v111 row_ror:1 row_mask:0xf bank_mask:0xf
	v_mov_b32_dpp v137, v111 row_ror:2 row_mask:0xf bank_mask:0xf
	v_pk_mul_f32 v[110:111], v[168:169], v[134:135] op_sel_hi:[0,1]
	v_mul_f32_e32 v134, 0xbfb8aa3b, v104
	v_exp_f32_e32 v207, v134
	v_mov_b32_dpp v136, v110 row_shr:2 row_mask:0xf bank_mask:0xf
	v_mov_b32_dpp v137, v111 row_shr:2 row_mask:0xf bank_mask:0xf
	v_mov_b32_dpp v128, v110 row_shr:1 row_mask:0xf bank_mask:0xf
	v_mov_b32_dpp v129, v111 row_shr:1 row_mask:0xf bank_mask:0xf
	v_pk_fma_f32 v[134:135], v[142:143], v[136:137], v[100:101]
	v_pk_fma_f32 v[130:131], v[108:109], v[226:227], v[130:131]
	v_pk_fma_f32 v[128:129], v[220:221], v[128:129], v[134:135]
	v_add_f32_e32 v134, 1.0, v207
	v_rcp_f32_e32 v134, v134
	v_mul_f32_e32 v135, 0xbfb8aa3b, v130
	v_exp_f32_e32 v135, v135
	v_pk_fma_f32 v[106:107], v[132:133], v[146:147], v[106:107]
	v_mul_f32_e32 v104, v104, v134
	v_pk_fma_f32 v[128:129], v[110:111], v[140:141], v[128:129]
	v_mul_f32_e32 v104, v104, v105
	v_add_f32_e32 v105, 1.0, v135
	v_mul_f32_e32 v134, 0xbfb8aa3b, v106
	v_rcp_f32_e32 v105, v105
	v_exp_f32_e32 v134, v134
	v_mul_f32_e32 v135, 0xbfb8aa3b, v128
	v_exp_f32_e32 v135, v135
	v_mul_f32_e32 v105, v130, v105
	v_add_f32_e32 v130, 1.0, v134
	v_rcp_f32_e32 v130, v130
	v_add_f32_e32 v134, 1.0, v135
	v_rcp_f32_e32 v134, v134
	v_mul_f32_e32 v105, v105, v131
	v_mul_f32_e32 v106, v106, v130
	v_mul_f32_e32 v106, v106, v107
	v_mul_f32_e32 v107, v128, v134
	v_mul_f32_e32 v107, v107, v129
	v_cvt_pk_bf16_f32 v104, v104, v105
	v_cvt_pk_bf16_f32 v105, v106, v107
	v_add_u32_e32 v106, 32, v169
	v_mad_u64_u32 v[128:129], s[34:35], v106, s72, v[138:139]
	s_nop 0
	s_nop 0
	global_store_dwordx2 v[128:129], v[104:105], off
	s_nop 0
	v_mov_b32_dpp v106, v232 row_ror:2 row_mask:0xf bank_mask:0xf
	s_nop 0
	v_mov_b32_dpp v107, v233 row_ror:2 row_mask:0xf bank_mask:0xf
	v_pk_mul_f32 v[234:235], v[174:175], v[190:191] op_sel_hi:[0,1]
	v_mov_b32_dpp v104, v232 row_ror:1 row_mask:0xf bank_mask:0xf
	v_mov_b32_dpp v105, v233 row_ror:1 row_mask:0xf bank_mask:0xf
	v_mov_b32_dpp v106, v234 row_shr:2 row_mask:0xf bank_mask:0xf
	v_mov_b32_dpp v107, v235 row_shr:2 row_mask:0xf bank_mask:0xf
	s_nop 0
	v_mov_b32_dpp v104, v234 row_shr:1 row_mask:0xf bank_mask:0xf
	v_mov_b32_dpp v105, v235 row_shr:1 row_mask:0xf bank_mask:0xf
	v_pk_fma_f32 v[106:107], v[112:113], v[106:107], v[114:115]
	s_nop 0
	s_nop 0
	v_mov_b32_dpp v134, v108 row_ror:2 row_mask:0xf bank_mask:0xf
	v_pk_fma_f32 v[104:105], v[116:117], v[104:105], v[106:107]
	s_nop 0
	v_mov_b32_dpp v135, v109 row_ror:2 row_mask:0xf bank_mask:0xf
	v_pk_mul_f32 v[106:107], v[174:175], v[186:187] op_sel_hi:[0,1]
	v_mov_b32_dpp v130, v108 row_ror:1 row_mask:0xf bank_mask:0xf
	v_mov_b32_dpp v131, v109 row_ror:1 row_mask:0xf bank_mask:0xf
	v_mov_b32_dpp v134, v106 row_shr:2 row_mask:0xf bank_mask:0xf
	v_mov_b32_dpp v135, v107 row_shr:2 row_mask:0xf bank_mask:0xf
	v_mov_b32_dpp v130, v106 row_shr:1 row_mask:0xf bank_mask:0xf
	v_mov_b32_dpp v131, v107 row_shr:1 row_mask:0xf bank_mask:0xf
	v_pk_fma_f32 v[134:135], v[222:223], v[134:135], v[98:99]
	s_nop 0
	v_pk_fma_f32 v[130:131], v[224:225], v[130:131], v[134:135]
	s_nop 0
	s_nop 0
	v_mov_b32_dpp v136, v132 row_ror:2 row_mask:0xf bank_mask:0xf
	v_pk_fma_f32 v[106:107], v[106:107], v[226:227], v[130:131]
	s_nop 0
	v_mov_b32_dpp v137, v133 row_ror:2 row_mask:0xf bank_mask:0xf
	v_pk_mul_f32 v[130:131], v[174:175], v[188:189] op_sel_hi:[0,1]
	v_mov_b32_dpp v108, v132 row_ror:1 row_mask:0xf bank_mask:0xf
	v_mov_b32_dpp v109, v133 row_ror:1 row_mask:0xf bank_mask:0xf
	v_mov_b32_dpp v136, v130 row_shr:2 row_mask:0xf bank_mask:0xf
	v_mov_b32_dpp v137, v131 row_shr:2 row_mask:0xf bank_mask:0xf
	v_mov_b32_dpp v108, v130 row_shr:1 row_mask:0xf bank_mask:0xf
	v_mov_b32_dpp v109, v131 row_shr:1 row_mask:0xf bank_mask:0xf
	v_pk_fma_f32 v[134:135], v[120:121], v[136:137], v[122:123]
	v_pk_fma_f32 v[104:105], v[234:235], v[118:119], v[104:105]
	v_pk_fma_f32 v[108:109], v[144:145], v[108:109], v[134:135]
	s_nop 0
	v_pk_fma_f32 v[108:109], v[130:131], v[146:147], v[108:109]
	v_mul_f32_e32 v130, 0xbfb8aa3b, v104
	s_nop 0
	s_nop 0
	s_nop 0
	v_exp_f32_e32 v134, v130
	v_mov_b32_dpp v132, v110 row_ror:1 row_mask:0xf bank_mask:0xf
	v_mov_b32_dpp v232, v110 row_ror:2 row_mask:0xf bank_mask:0xf
	v_mov_b32_dpp v133, v111 row_ror:1 row_mask:0xf bank_mask:0xf
	v_mov_b32_dpp v233, v111 row_ror:2 row_mask:0xf bank_mask:0xf
	v_pk_mul_f32 v[110:111], v[174:175], v[184:185] op_sel_hi:[0,1]
	v_add_u32_e32 v103, s61, v103
	v_mov_b32_e32 v102, 0
	v_mov_b32_dpp v232, v110 row_shr:2 row_mask:0xf bank_mask:0xf
	v_mov_b32_dpp v233, v111 row_shr:2 row_mask:0xf bank_mask:0xf
	v_mov_b32_dpp v132, v110 row_shr:1 row_mask:0xf bank_mask:0xf
	v_mov_b32_dpp v133, v111 row_shr:1 row_mask:0xf bank_mask:0xf
	v_pk_fma_f32 v[130:131], v[142:143], v[232:233], v[100:101]
	v_lshl_add_u32 v195, v103, 9, v195
	v_pk_fma_f32 v[130:131], v[220:221], v[132:133], v[130:131]
	v_add_f32_e32 v132, 1.0, v134
	v_rcp_f32_e32 v132, v132
	v_mul_f32_e32 v133, 0xbfb8aa3b, v106
	v_exp_f32_e32 v133, v133
	v_pk_fma_f32 v[110:111], v[110:111], v[140:141], v[130:131]
	v_mul_f32_e32 v104, v104, v132
	v_mul_f32_e32 v104, v104, v105
	v_add_f32_e32 v105, 1.0, v133
	v_mul_f32_e32 v130, 0xbfb8aa3b, v108
	v_rcp_f32_e32 v105, v105
	v_exp_f32_e32 v130, v130
	v_mul_f32_e32 v131, 0xbfb8aa3b, v110
	v_exp_f32_e32 v131, v131
	v_mul_f32_e32 v105, v106, v105
	v_add_f32_e32 v106, 1.0, v130
	v_rcp_f32_e32 v106, v106
	v_add_f32_e32 v130, 1.0, v131
	v_rcp_f32_e32 v130, v130
	v_mul_f32_e32 v105, v105, v107
	v_mul_f32_e32 v106, v108, v106
	v_mul_f32_e32 v106, v106, v109
	v_mul_f32_e32 v107, v110, v130
	v_mul_f32_e32 v107, v107, v111
	v_cvt_pk_bf16_f32 v104, v104, v105
	v_cvt_pk_bf16_f32 v105, v106, v107
	v_add_u32_e32 v106, 48, v169
	v_mad_u64_u32 v[132:133], s[34:35], v106, s72, v[138:139]
	v_mov_b32_e32 v106, 0
	v_mov_b32_e32 v107, 0
	v_mov_b32_e32 v108, 0
	v_mov_b32_e32 v109, 0
	global_store_dwordx2 v[132:133], v[104:105], off
	s_and_saveexec_b64 s[34:35], vcc
	ds_read_b128 v[106:109], v195
	s_or_b64 exec, exec, s[34:35]
	v_mov_b32_e32 v103, 0
	v_mov_b32_e32 v104, 0
	v_mov_b32_e32 v105, 0
	s_and_saveexec_b64 s[34:35], vcc
	ds_read_b128 v[102:105], v195 offset:512
	s_or_b64 exec, exec, s[34:35]
	v_cvt_f32_i32_e32 v237, v90
	v_cvt_f32_i32_e32 v91, v91
	v_cvt_f32_i32_e32 v90, v95
	v_cvt_f32_i32_e32 v236, v94
	s_nop 0
	s_nop 0
	s_nop 0
	s_waitcnt lgkmcnt(0)
	v_mov_b32_dpp v110, v106 row_ror:1 row_mask:0xf bank_mask:0xf
	v_mov_b32_dpp v130, v106 row_ror:2 row_mask:0xf bank_mask:0xf
	s_nop 0
	s_nop 0
	v_mov_b32_dpp v134, v107 row_ror:2 row_mask:0xf bank_mask:0xf
	v_mov_b32_dpp v106, v107 row_ror:1 row_mask:0xf bank_mask:0xf
	s_nop 0
	s_nop 0
	s_nop 0
	v_mov_b32_dpp v135, v103 row_ror:2 row_mask:0xf bank_mask:0xf
	v_pk_mul_f32 v[90:91], v[208:209], v[90:91] op_sel_hi:[0,1]
	v_mov_b32_dpp v111, v102 row_ror:1 row_mask:0xf bank_mask:0xf
	v_mov_b32_dpp v131, v102 row_ror:2 row_mask:0xf bank_mask:0xf
	v_pk_mul_f32 v[236:237], v[208:209], v[236:237] op_sel_hi:[0,1]
	v_mov_b32_dpp v107, v103 row_ror:1 row_mask:0xf bank_mask:0xf
	v_mov_b32_dpp v134, v90 row_shr:2 row_mask:0xf bank_mask:0xf
	v_mov_b32_dpp v135, v91 row_shr:2 row_mask:0xf bank_mask:0xf
	v_cvt_f32_i32_e32 v103, v92
	v_cvt_f32_i32_e32 v102, v96
	v_cvt_f32_i32_e32 v93, v93
	v_cvt_f32_i32_e32 v92, v97
	s_nop 0
	s_nop 0
	v_mov_b32_dpp v130, v236 row_shr:2 row_mask:0xf bank_mask:0xf
	v_mov_b32_dpp v131, v237 row_shr:2 row_mask:0xf bank_mask:0xf
	v_mov_b32_dpp v106, v90 row_shr:1 row_mask:0xf bank_mask:0xf
	v_mov_b32_dpp v107, v91 row_shr:1 row_mask:0xf bank_mask:0xf
	v_pk_fma_f32 v[94:95], v[222:223], v[134:135], v[98:99]
	v_mov_b32_dpp v136, v108 row_ror:1 row_mask:0xf bank_mask:0xf
	v_mov_b32_dpp v232, v108 row_ror:2 row_mask:0xf bank_mask:0xf
	s_nop 0
	s_nop 0
	v_mov_b32_dpp v110, v236 row_shr:1 row_mask:0xf bank_mask:0xf
	v_mov_b32_dpp v111, v237 row_shr:1 row_mask:0xf bank_mask:0xf
	v_pk_fma_f32 v[130:131], v[112:113], v[130:131], v[114:115]
	v_pk_fma_f32 v[94:95], v[224:225], v[106:107], v[94:95]
	v_mov_b32_dpp v108, v109 row_ror:1 row_mask:0xf bank_mask:0xf
	v_mov_b32_dpp v234, v109 row_ror:2 row_mask:0xf bank_mask:0xf
	v_pk_fma_f32 v[110:111], v[116:117], v[110:111], v[130:131]
	v_pk_fma_f32 v[94:95], v[90:91], v[226:227], v[94:95]
	s_nop 0
	s_nop 0
	s_nop 0
	v_pk_fma_f32 v[110:111], v[236:237], v[118:119], v[110:111]
	s_nop 0
	v_mov_b32_dpp v233, v104 row_ror:2 row_mask:0xf bank_mask:0xf
	v_pk_mul_f32 v[102:103], v[208:209], v[102:103] op_sel_hi:[0,1]
	v_mov_b32_dpp v109, v105 row_ror:1 row_mask:0xf bank_mask:0xf
	v_mov_b32_dpp v235, v105 row_ror:2 row_mask:0xf bank_mask:0xf
	v_pk_mul_f32 v[92:93], v[208:209], v[92:93] op_sel_hi:[0,1]
	v_mul_f32_e32 v105, 0xbfb8aa3b, v94
	v_mov_b32_dpp v137, v104 row_ror:1 row_mask:0xf bank_mask:0xf
	v_mov_b32_dpp v232, v102 row_shr:2 row_mask:0xf bank_mask:0xf
	v_mov_b32_dpp v233, v103 row_shr:2 row_mask:0xf bank_mask:0xf
	v_mov_b32_dpp v234, v92 row_shr:2 row_mask:0xf bank_mask:0xf
	v_mul_f32_e32 v96, 0xbfb8aa3b, v110
	v_mov_b32_dpp v235, v93 row_shr:2 row_mask:0xf bank_mask:0xf
	v_exp_f32_e32 v105, v105
	v_mov_b32_dpp v136, v102 row_shr:1 row_mask:0xf bank_mask:0xf
	v_mov_b32_dpp v137, v103 row_shr:1 row_mask:0xf bank_mask:0xf
	v_pk_fma_f32 v[106:107], v[120:121], v[232:233], v[122:123]
	v_mov_b32_dpp v108, v92 row_shr:1 row_mask:0xf bank_mask:0xf
	v_mov_b32_dpp v109, v93 row_shr:1 row_mask:0xf bank_mask:0xf
	v_exp_f32_e32 v104, v96
	v_pk_fma_f32 v[96:97], v[142:143], v[234:235], v[100:101]
	v_pk_fma_f32 v[106:107], v[144:145], v[136:137], v[106:107]
	v_pk_fma_f32 v[96:97], v[220:221], v[108:109], v[96:97]
	v_pk_fma_f32 v[106:107], v[102:103], v[146:147], v[106:107]
	v_pk_fma_f32 v[96:97], v[92:93], v[140:141], v[96:97]
	v_add_f32_e32 v105, 1.0, v105
	v_mul_f32_e32 v108, 0xbfb8aa3b, v106
	v_mul_f32_e32 v109, 0xbfb8aa3b, v96
	v_rcp_f32_e32 v105, v105
	v_exp_f32_e32 v108, v108
	v_exp_f32_e32 v109, v109
	v_add_f32_e32 v104, 1.0, v104
	v_mul_f32_e32 v94, v94, v105
	v_add_f32_e32 v105, 1.0, v108
	v_add_f32_e32 v108, 1.0, v109
	v_rcp_f32_e32 v105, v105
	v_rcp_f32_e32 v108, v108
	v_rcp_f32_e32 v104, v104
	v_cvt_f32_i32_e32 v135, v82
	v_cvt_f32_i32_e32 v134, v86
	v_mul_f32_e32 v94, v94, v95
	v_mul_f32_e32 v95, v106, v105
	v_mul_f32_e32 v96, v96, v108
	v_add_u32_e32 v207, 0x80, v169
	v_mul_f32_e32 v104, v110, v104
	v_mul_f32_e32 v95, v95, v107
	v_mul_f32_e32 v96, v96, v97
	v_mul_f32_e32 v104, v104, v111
	v_cvt_pk_bf16_f32 v94, v104, v94
	v_cvt_pk_bf16_f32 v95, v95, v96
	v_mad_u64_u32 v[130:131], s[34:35], v207, s72, v[138:139]
	s_nop 0
	s_nop 0
	global_store_dwordx2 v[130:131], v[94:95], off
	s_nop 0
	v_mov_b32_dpp v96, v236 row_ror:2 row_mask:0xf bank_mask:0xf
	s_nop 0
	v_mov_b32_dpp v97, v237 row_ror:2 row_mask:0xf bank_mask:0xf
	v_pk_mul_f32 v[136:137], v[206:207], v[134:135] op_sel_hi:[0,1]
	v_mov_b32_dpp v94, v236 row_ror:1 row_mask:0xf bank_mask:0xf
	v_mov_b32_dpp v95, v237 row_ror:1 row_mask:0xf bank_mask:0xf
	v_mov_b32_dpp v96, v136 row_shr:2 row_mask:0xf bank_mask:0xf
	v_mov_b32_dpp v97, v137 row_shr:2 row_mask:0xf bank_mask:0xf
	v_mov_b32_dpp v94, v136 row_shr:1 row_mask:0xf bank_mask:0xf
	v_mov_b32_dpp v95, v137 row_shr:1 row_mask:0xf bank_mask:0xf
	v_pk_fma_f32 v[96:97], v[112:113], v[96:97], v[114:115]
	v_cvt_f32_i32_e32 v83, v83
	v_cvt_f32_i32_e32 v82, v87
	s_nop 0
	s_nop 0
	v_pk_fma_f32 v[94:95], v[116:117], v[94:95], v[96:97]
	v_mov_b32_dpp v104, v90 row_ror:1 row_mask:0xf bank_mask:0xf
	v_mov_b32_dpp v106, v90 row_ror:2 row_mask:0xf bank_mask:0xf
	s_nop 0
	s_nop 0
	v_pk_fma_f32 v[94:95], v[136:137], v[118:119], v[94:95]
	v_mov_b32_dpp v90, v102 row_ror:1 row_mask:0xf bank_mask:0xf
	v_mov_b32_dpp v108, v102 row_ror:2 row_mask:0xf bank_mask:0xf
	s_nop 0
	s_nop 0
	s_nop 0
	v_cvt_f32_i32_e32 v96, v88
	v_mul_f32_e32 v88, 0xbfb8aa3b, v94
	v_mov_b32_dpp v102, v92 row_ror:1 row_mask:0xf bank_mask:0xf
	v_mov_b32_dpp v110, v92 row_ror:2 row_mask:0xf bank_mask:0xf
	s_nop 0
	v_mov_b32_dpp v107, v91 row_ror:2 row_mask:0xf bank_mask:0xf
	v_pk_mul_f32 v[82:83], v[206:207], v[82:83] op_sel_hi:[0,1]
	v_exp_f32_e32 v92, v88
	v_mov_b32_dpp v105, v91 row_ror:1 row_mask:0xf bank_mask:0xf
	v_mov_b32_dpp v106, v82 row_shr:2 row_mask:0xf bank_mask:0xf
	v_mov_b32_dpp v107, v83 row_shr:2 row_mask:0xf bank_mask:0xf
	v_cvt_f32_i32_e32 v97, v84
	v_cvt_f32_i32_e32 v85, v85
	v_cvt_f32_i32_e32 v84, v89
	v_mov_b32_dpp v104, v82 row_shr:1 row_mask:0xf bank_mask:0xf
	v_mov_b32_dpp v105, v83 row_shr:1 row_mask:0xf bank_mask:0xf
	v_pk_fma_f32 v[86:87], v[222:223], v[106:107], v[98:99]
	s_nop 0
	v_pk_fma_f32 v[86:87], v[224:225], v[104:105], v[86:87]
	s_nop 0
	v_pk_fma_f32 v[86:87], v[82:83], v[226:227], v[86:87]
	v_mov_b32_dpp v91, v103 row_ror:1 row_mask:0xf bank_mask:0xf
	v_mov_b32_dpp v109, v103 row_ror:2 row_mask:0xf bank_mask:0xf
	s_nop 0
	s_nop 0
	v_add_f32_e32 v92, 1.0, v92
	v_pk_mul_f32 v[96:97], v[206:207], v[96:97] op_sel_hi:[0,1]
	v_mov_b32_dpp v103, v93 row_ror:1 row_mask:0xf bank_mask:0xf
	v_mov_b32_dpp v111, v93 row_ror:2 row_mask:0xf bank_mask:0xf
	v_pk_mul_f32 v[84:85], v[206:207], v[84:85] op_sel_hi:[0,1]
	v_rcp_f32_e32 v92, v92
	v_mul_f32_e32 v93, 0xbfb8aa3b, v86
	v_mov_b32_dpp v108, v96 row_shr:2 row_mask:0xf bank_mask:0xf
	v_mov_b32_dpp v109, v97 row_shr:2 row_mask:0xf bank_mask:0xf
	v_mov_b32_dpp v110, v84 row_shr:2 row_mask:0xf bank_mask:0xf
	v_mov_b32_dpp v111, v85 row_shr:2 row_mask:0xf bank_mask:0xf
	v_exp_f32_e32 v93, v93
	v_mov_b32_dpp v90, v96 row_shr:1 row_mask:0xf bank_mask:0xf
	v_mov_b32_dpp v91, v97 row_shr:1 row_mask:0xf bank_mask:0xf
	v_pk_fma_f32 v[104:105], v[120:121], v[108:109], v[122:123]
	v_mov_b32_dpp v102, v84 row_shr:1 row_mask:0xf bank_mask:0xf
	v_mov_b32_dpp v103, v85 row_shr:1 row_mask:0xf bank_mask:0xf
	v_pk_fma_f32 v[88:89], v[142:143], v[110:111], v[100:101]
	v_pk_fma_f32 v[90:91], v[144:145], v[90:91], v[104:105]
	v_pk_fma_f32 v[88:89], v[220:221], v[102:103], v[88:89]
	v_pk_fma_f32 v[90:91], v[96:97], v[146:147], v[90:91]
	v_pk_fma_f32 v[88:89], v[84:85], v[140:141], v[88:89]
	v_mul_f32_e32 v92, v94, v92
	v_mul_f32_e32 v92, v92, v95
	v_add_f32_e32 v93, 1.0, v93
	v_mul_f32_e32 v94, 0xbfb8aa3b, v90
	v_mul_f32_e32 v95, 0xbfb8aa3b, v88
	v_rcp_f32_e32 v93, v93
	v_exp_f32_e32 v94, v94
	v_exp_f32_e32 v95, v95
	v_cvt_f32_i32_e32 v105, v74
	v_mul_f32_e32 v86, v86, v93
	v_add_f32_e32 v93, 1.0, v94
	v_add_f32_e32 v94, 1.0, v95
	v_rcp_f32_e32 v93, v93
	v_rcp_f32_e32 v94, v94
	v_mul_f32_e32 v86, v86, v87
	v_cvt_f32_i32_e32 v104, v78
	v_mul_f32_e32 v87, v90, v93
	v_mul_f32_e32 v88, v88, v94
	v_mul_f32_e32 v87, v87, v91
	v_mul_f32_e32 v88, v88, v89
	v_cvt_pk_bf16_f32 v86, v92, v86
	v_cvt_pk_bf16_f32 v87, v87, v88
	v_add_u32_e32 v88, 0x90, v169
	v_mad_u64_u32 v[134:135], s[34:35], v88, s72, v[138:139]
	s_nop 0
	s_nop 0
	global_store_dwordx2 v[134:135], v[86:87], off
	s_nop 0
	v_mov_b32_dpp v88, v136 row_ror:2 row_mask:0xf bank_mask:0xf
	s_nop 0
	v_mov_b32_dpp v89, v137 row_ror:2 row_mask:0xf bank_mask:0xf
	v_pk_mul_f32 v[104:105], v[198:199], v[104:105] op_sel_hi:[0,1]
	v_mov_b32_dpp v86, v136 row_ror:1 row_mask:0xf bank_mask:0xf
	v_mov_b32_dpp v87, v137 row_ror:1 row_mask:0xf bank_mask:0xf
	v_mov_b32_dpp v88, v104 row_shr:2 row_mask:0xf bank_mask:0xf
	v_mov_b32_dpp v89, v105 row_shr:2 row_mask:0xf bank_mask:0xf
	v_mov_b32_dpp v86, v104 row_shr:1 row_mask:0xf bank_mask:0xf
	v_mov_b32_dpp v87, v105 row_shr:1 row_mask:0xf bank_mask:0xf
	v_pk_fma_f32 v[88:89], v[112:113], v[88:89], v[114:115]
	v_cvt_f32_i32_e32 v75, v75
	v_cvt_f32_i32_e32 v74, v79
	s_nop 0
	s_nop 0
	v_pk_fma_f32 v[86:87], v[116:117], v[86:87], v[88:89]
	v_mov_b32_dpp v90, v82 row_ror:1 row_mask:0xf bank_mask:0xf
	v_mov_b32_dpp v92, v82 row_ror:2 row_mask:0xf bank_mask:0xf
	s_nop 0
	s_nop 0
	v_pk_fma_f32 v[86:87], v[104:105], v[118:119], v[86:87]
	v_mov_b32_dpp v82, v96 row_ror:1 row_mask:0xf bank_mask:0xf
	v_mov_b32_dpp v94, v96 row_ror:2 row_mask:0xf bank_mask:0xf
	s_nop 0
	s_nop 0
	s_nop 0
	v_cvt_f32_i32_e32 v88, v80
	v_mul_f32_e32 v80, 0xbfb8aa3b, v86
	v_mov_b32_dpp v96, v84 row_ror:1 row_mask:0xf bank_mask:0xf
	v_mov_b32_dpp v102, v84 row_ror:2 row_mask:0xf bank_mask:0xf
	s_nop 0
	v_mov_b32_dpp v93, v83 row_ror:2 row_mask:0xf bank_mask:0xf
	v_pk_mul_f32 v[74:75], v[198:199], v[74:75] op_sel_hi:[0,1]
	v_exp_f32_e32 v84, v80
	v_mov_b32_dpp v91, v83 row_ror:1 row_mask:0xf bank_mask:0xf
	v_mov_b32_dpp v92, v74 row_shr:2 row_mask:0xf bank_mask:0xf
	v_mov_b32_dpp v93, v75 row_shr:2 row_mask:0xf bank_mask:0xf
	v_cvt_f32_i32_e32 v89, v76
	v_cvt_f32_i32_e32 v77, v77
	v_cvt_f32_i32_e32 v76, v81
	v_mov_b32_dpp v90, v74 row_shr:1 row_mask:0xf bank_mask:0xf
	v_mov_b32_dpp v91, v75 row_shr:1 row_mask:0xf bank_mask:0xf
	v_pk_fma_f32 v[78:79], v[222:223], v[92:93], v[98:99]
	s_nop 0
	v_pk_fma_f32 v[78:79], v[224:225], v[90:91], v[78:79]
	s_nop 0
	v_pk_fma_f32 v[78:79], v[74:75], v[226:227], v[78:79]
	v_mov_b32_dpp v83, v97 row_ror:1 row_mask:0xf bank_mask:0xf
	v_mov_b32_dpp v95, v97 row_ror:2 row_mask:0xf bank_mask:0xf
	s_nop 0
	s_nop 0
	v_add_f32_e32 v84, 1.0, v84
	v_pk_mul_f32 v[88:89], v[198:199], v[88:89] op_sel_hi:[0,1]
	v_mov_b32_dpp v97, v85 row_ror:1 row_mask:0xf bank_mask:0xf
	v_mov_b32_dpp v103, v85 row_ror:2 row_mask:0xf bank_mask:0xf
	v_pk_mul_f32 v[76:77], v[198:199], v[76:77] op_sel_hi:[0,1]
	v_rcp_f32_e32 v84, v84
	v_mul_f32_e32 v85, 0xbfb8aa3b, v78
	v_mov_b32_dpp v94, v88 row_shr:2 row_mask:0xf bank_mask:0xf
	v_mov_b32_dpp v95, v89 row_shr:2 row_mask:0xf bank_mask:0xf
	v_mov_b32_dpp v102, v76 row_shr:2 row_mask:0xf bank_mask:0xf
	v_mov_b32_dpp v103, v77 row_shr:2 row_mask:0xf bank_mask:0xf
	v_exp_f32_e32 v85, v85
	v_mov_b32_dpp v82, v88 row_shr:1 row_mask:0xf bank_mask:0xf
	v_mov_b32_dpp v83, v89 row_shr:1 row_mask:0xf bank_mask:0xf
	v_pk_fma_f32 v[90:91], v[120:121], v[94:95], v[122:123]
	v_mov_b32_dpp v96, v76 row_shr:1 row_mask:0xf bank_mask:0xf
	v_mov_b32_dpp v97, v77 row_shr:1 row_mask:0xf bank_mask:0xf
	v_pk_fma_f32 v[80:81], v[142:143], v[102:103], v[100:101]
	v_pk_fma_f32 v[82:83], v[144:145], v[82:83], v[90:91]
	v_pk_fma_f32 v[80:81], v[220:221], v[96:97], v[80:81]
	v_pk_fma_f32 v[82:83], v[88:89], v[146:147], v[82:83]
	v_pk_fma_f32 v[80:81], v[76:77], v[140:141], v[80:81]
	v_mul_f32_e32 v84, v86, v84
	v_mul_f32_e32 v84, v84, v87
	v_add_f32_e32 v85, 1.0, v85
	v_mul_f32_e32 v86, 0xbfb8aa3b, v82
	v_mul_f32_e32 v87, 0xbfb8aa3b, v80
	v_rcp_f32_e32 v85, v85
	v_exp_f32_e32 v86, v86
	v_exp_f32_e32 v87, v87
	v_pk_mul_f32 v[92:93], v[194:195], v[218:219] op_sel_hi:[0,1]
	v_mul_f32_e32 v78, v78, v85
	v_add_f32_e32 v85, 1.0, v86
	v_add_f32_e32 v86, 1.0, v87
	v_rcp_f32_e32 v85, v85
	v_rcp_f32_e32 v86, v86
	v_mul_f32_e32 v78, v78, v79
	v_cvt_pk_bf16_f32 v78, v84, v78
	v_mul_f32_e32 v79, v82, v85
	v_mul_f32_e32 v80, v80, v86
	v_mul_f32_e32 v79, v79, v83
	v_mul_f32_e32 v80, v80, v81
	v_cvt_pk_bf16_f32 v79, v79, v80
	v_add_u32_e32 v80, 0xa0, v169
	v_mad_u64_u32 v[136:137], s[34:35], v80, s72, v[138:139]
	s_nop 0
	s_nop 0
	global_store_dwordx2 v[136:137], v[78:79], off
	s_nop 0
	v_mov_b32_dpp v80, v104 row_ror:2 row_mask:0xf bank_mask:0xf
	s_nop 0
	v_mov_b32_dpp v81, v105 row_ror:2 row_mask:0xf bank_mask:0xf
	v_mov_b32_dpp v78, v104 row_ror:1 row_mask:0xf bank_mask:0xf
	v_mov_b32_dpp v79, v105 row_ror:1 row_mask:0xf bank_mask:0xf
	v_mov_b32_dpp v80, v92 row_shr:2 row_mask:0xf bank_mask:0xf
	v_mov_b32_dpp v81, v93 row_shr:2 row_mask:0xf bank_mask:0xf
	s_nop 0
	v_mov_b32_dpp v78, v92 row_shr:1 row_mask:0xf bank_mask:0xf
	v_mov_b32_dpp v79, v93 row_shr:1 row_mask:0xf bank_mask:0xf
	v_pk_fma_f32 v[80:81], v[112:113], v[80:81], v[114:115]
	s_nop 0
	s_nop 0
	v_mov_b32_dpp v84, v74 row_ror:2 row_mask:0xf bank_mask:0xf
	v_pk_fma_f32 v[78:79], v[116:117], v[78:79], v[80:81]
	s_nop 0
	v_mov_b32_dpp v85, v75 row_ror:2 row_mask:0xf bank_mask:0xf
	v_pk_mul_f32 v[80:81], v[194:195], v[216:217] op_sel_hi:[0,1]
	v_mov_b32_dpp v82, v74 row_ror:1 row_mask:0xf bank_mask:0xf
	v_mov_b32_dpp v83, v75 row_ror:1 row_mask:0xf bank_mask:0xf
	v_mov_b32_dpp v84, v80 row_shr:2 row_mask:0xf bank_mask:0xf
	v_mov_b32_dpp v85, v81 row_shr:2 row_mask:0xf bank_mask:0xf
	v_mov_b32_dpp v82, v80 row_shr:1 row_mask:0xf bank_mask:0xf
	v_mov_b32_dpp v83, v81 row_shr:1 row_mask:0xf bank_mask:0xf
	v_pk_fma_f32 v[84:85], v[222:223], v[84:85], v[98:99]
	s_nop 0
	v_pk_fma_f32 v[82:83], v[224:225], v[82:83], v[84:85]
	s_nop 0
	s_nop 0
	v_mov_b32_dpp v86, v88 row_ror:2 row_mask:0xf bank_mask:0xf
	v_pk_fma_f32 v[80:81], v[80:81], v[226:227], v[82:83]
	s_nop 0
	v_mov_b32_dpp v87, v89 row_ror:2 row_mask:0xf bank_mask:0xf
	v_pk_mul_f32 v[82:83], v[194:195], v[214:215] op_sel_hi:[0,1]
	v_mov_b32_dpp v74, v88 row_ror:1 row_mask:0xf bank_mask:0xf
	v_mov_b32_dpp v75, v89 row_ror:1 row_mask:0xf bank_mask:0xf
	v_mov_b32_dpp v86, v82 row_shr:2 row_mask:0xf bank_mask:0xf
	v_mov_b32_dpp v87, v83 row_shr:2 row_mask:0xf bank_mask:0xf
	v_mov_b32_dpp v74, v82 row_shr:1 row_mask:0xf bank_mask:0xf
	v_mov_b32_dpp v75, v83 row_shr:1 row_mask:0xf bank_mask:0xf
	v_pk_fma_f32 v[84:85], v[120:121], v[86:87], v[122:123]
	v_pk_fma_f32 v[78:79], v[92:93], v[118:119], v[78:79]
	v_pk_fma_f32 v[74:75], v[144:145], v[74:75], v[84:85]
	s_nop 0
	v_pk_fma_f32 v[74:75], v[82:83], v[146:147], v[74:75]
	v_mul_f32_e32 v82, 0xbfb8aa3b, v78
	v_exp_f32_e32 v84, v82
	s_nop 0
	s_nop 0
	s_nop 0
	v_add_f32_e32 v84, 1.0, v84
	v_rcp_f32_e32 v84, v84
	v_mul_f32_e32 v85, 0xbfb8aa3b, v80
	v_mov_b32_dpp v88, v76 row_ror:1 row_mask:0xf bank_mask:0xf
	v_mov_b32_dpp v90, v76 row_ror:2 row_mask:0xf bank_mask:0xf
	v_mov_b32_dpp v89, v77 row_ror:1 row_mask:0xf bank_mask:0xf
	v_mov_b32_dpp v91, v77 row_ror:2 row_mask:0xf bank_mask:0xf
	v_pk_mul_f32 v[76:77], v[194:195], v[210:211] op_sel_hi:[0,1]
	v_exp_f32_e32 v85, v85
	v_mul_f32_e32 v78, v78, v84
	v_mov_b32_dpp v90, v76 row_shr:2 row_mask:0xf bank_mask:0xf
	v_mov_b32_dpp v91, v77 row_shr:2 row_mask:0xf bank_mask:0xf
	v_mov_b32_dpp v88, v76 row_shr:1 row_mask:0xf bank_mask:0xf
	v_mov_b32_dpp v89, v77 row_shr:1 row_mask:0xf bank_mask:0xf
	v_pk_fma_f32 v[82:83], v[142:143], v[90:91], v[100:101]
	v_mul_f32_e32 v78, v78, v79
	v_pk_fma_f32 v[82:83], v[220:221], v[88:89], v[82:83]
	v_add_f32_e32 v79, 1.0, v85
	v_pk_fma_f32 v[76:77], v[76:77], v[140:141], v[82:83]
	v_mul_f32_e32 v82, 0xbfb8aa3b, v74
	v_rcp_f32_e32 v79, v79
	v_exp_f32_e32 v82, v82
	v_mul_f32_e32 v83, 0xbfb8aa3b, v76
	v_exp_f32_e32 v83, v83
	v_mul_f32_e32 v79, v80, v79
	v_add_f32_e32 v80, 1.0, v82
	v_rcp_f32_e32 v80, v80
	v_add_f32_e32 v82, 1.0, v83
	v_rcp_f32_e32 v82, v82
	v_mul_f32_e32 v79, v79, v81
	v_mul_f32_e32 v74, v74, v80
	v_mul_f32_e32 v74, v74, v75
	v_mul_f32_e32 v75, v76, v82
	v_mul_f32_e32 v75, v75, v77
	v_cvt_pk_bf16_f32 v76, v78, v79
	v_cvt_pk_bf16_f32 v77, v74, v75
	v_or_b32_e32 v74, 1, v199
	v_lshl_add_u32 v74, v74, 4, 0
	v_add_u32_e32 v75, 0x22400, v74
	v_add_u32_e32 v78, 0x22000, v74
	ds_read_b128 v[88:91], v75
	ds_read_b128 v[80:83], v78
	ds_read_b128 v[100:103], v78 offset:2048
	ds_read_b128 v[96:99], v78 offset:3072
	ds_read_b128 v[92:95], v78 offset:4096
	v_add_u32_e32 v75, 0xb0, v169
	v_mad_u64_u32 v[138:139], s[34:35], v75, s72, v[138:139]
	global_store_dwordx2 v[138:139], v[76:77], off
	s_and_saveexec_b64 s[34:35], s[0:1]
	s_cbranch_execz .LBB0_1679
	v_cvt_f32_i32_e32 v77, v37
	v_cvt_f32_i32_e32 v85, v35
	v_cvt_f32_i32_e32 v84, v34
	v_cvt_f32_i32_e32 v76, v36
	v_pk_mul_f32 v[84:85], v[172:173], v[84:85] op_sel_hi:[0,1]
	v_pk_mul_f32 v[76:77], v[172:173], v[76:77] op_sel_hi:[0,1]
	s_waitcnt lgkmcnt(4)
	v_pk_mul_f32 v[86:87], v[76:77], v[90:91]
	v_pk_mul_f32 v[84:85], v[84:85], v[88:89]
	v_mad_i64_i32 v[76:77], s[38:39], v173, s73, v[212:213]
	global_store_dwordx4 v[76:77], v[84:87], off offset:16

.LBB0_1681:
	s_or_b64 exec, exec, s[34:35]
	s_nop 0
	v_mov_b32_e32 v84, 0
	v_mov_b32_e32 v112, 0
	v_mov_b32_e32 v113, 0
	v_mov_b32_e32 v114, 0
	v_mov_b32_e32 v115, 0
	s_and_saveexec_b64 s[0:1], s[40:41]
	ds_read_b128 v[112:115], v171 offset:16
	s_or_b64 exec, exec, s[0:1]
	v_mov_b32_e32 v85, 0
	v_mov_b32_e32 v86, 0
	v_mov_b32_e32 v87, 0
	s_and_saveexec_b64 s[0:1], s[40:41]
	ds_read_b128 v[84:87], v171 offset:528
	s_or_b64 exec, exec, s[0:1]
	s_waitcnt lgkmcnt(3)
	v_pk_mul_f32 v[122:123], v[106:107], v[122:123]
	s_waitcnt lgkmcnt(2)
	v_pk_mul_f32 v[118:119], v[106:107], v[118:119]
	s_waitcnt lgkmcnt(0)
	v_pk_mul_f32 v[106:107], v[106:107], v[110:111]
	v_pk_mul_f32 v[100:101], v[88:89], v[100:101]
	v_pk_mul_f32 v[110:111], v[90:91], v[98:99]
	v_pk_mul_f32 v[96:97], v[88:89], v[96:97]
	v_pk_mul_f32 v[98:99], v[88:89], v[92:93]
	v_cvt_f32_i32_e32 v89, v10
	v_cvt_f32_i32_e32 v88, v34
	v_mov_b32_e32 v173, v172
	s_nop 0
	s_nop 0
	v_pk_mul_f32 v[120:121], v[104:105], v[120:121]
	v_mov_b32_dpp v92, v112 row_ror:2 row_mask:0xf bank_mask:0xf
	v_mov_b32_dpp v93, v84 row_ror:2 row_mask:0xf bank_mask:0xf
	v_pk_mul_f32 v[210:211], v[172:173], v[88:89]
	v_cvt_f32_i32_e32 v215, v11
	v_cvt_f32_i32_e32 v214, v35
	v_pk_mul_f32 v[116:117], v[104:105], v[116:117]
	v_pk_mul_f32 v[104:105], v[104:105], v[108:109]
	v_pk_mul_f32 v[108:109], v[90:91], v[102:103]
	v_pk_mul_f32 v[140:141], v[90:91], v[94:95]
	s_nop 0
	v_mov_b32_dpp v92, v210 row_shr:2 row_mask:0xf bank_mask:0xf
	v_mov_b32_dpp v93, v211 row_shr:2 row_mask:0xf bank_mask:0xf
	v_mov_b32_e32 v88, v100
	v_mov_b32_e32 v89, v120
	v_mov_b32_e32 v90, v80
	v_mov_b32_e32 v91, v74
	v_mov_b32_dpp v94, v112 row_ror:1 row_mask:0xf bank_mask:0xf
	s_nop 0
	s_nop 0
	v_pk_fma_f32 v[212:213], v[88:89], v[92:93], v[90:91]
	v_mov_b32_e32 v92, v96
	v_mov_b32_e32 v93, v116
	v_mov_b32_e32 v116, v97
	v_cvt_f32_i32_e32 v97, v12
	v_cvt_f32_i32_e32 v96, v36
	v_mov_b32_dpp v102, v113 row_ror:1 row_mask:0xf bank_mask:0xf
	v_mov_b32_dpp v112, v113 row_ror:2 row_mask:0xf bank_mask:0xf
	s_nop 0
	s_nop 0
	s_nop 0
	v_mov_b32_dpp v95, v84 row_ror:1 row_mask:0xf bank_mask:0xf
	v_mov_b32_dpp v103, v85 row_ror:1 row_mask:0xf bank_mask:0xf
	v_mov_b32_dpp v113, v85 row_ror:2 row_mask:0xf bank_mask:0xf
	v_pk_mul_f32 v[84:85], v[172:173], v[214:215]
	s_nop 0
	v_mov_b32_e32 v120, v101
	v_mov_b32_dpp v112, v84 row_shr:2 row_mask:0xf bank_mask:0xf
	v_mov_b32_dpp v113, v85 row_shr:2 row_mask:0xf bank_mask:0xf
	v_mov_b32_e32 v74, v81
	s_nop 0
	v_mov_b32_dpp v144, v114 row_ror:2 row_mask:0xf bank_mask:0xf
	v_mov_b32_dpp v94, v210 row_shr:1 row_mask:0xf bank_mask:0xf
	v_mov_b32_dpp v95, v211 row_shr:1 row_mask:0xf bank_mask:0xf
	v_pk_fma_f32 v[80:81], v[120:121], v[112:113], v[74:75]
	v_mov_b32_dpp v145, v86 row_ror:2 row_mask:0xf bank_mask:0xf
	v_pk_mul_f32 v[112:113], v[172:173], v[96:97]
	v_pk_fma_f32 v[212:213], v[92:93], v[94:95], v[212:213]
	v_mov_b32_e32 v94, v98
	v_mov_b32_e32 v95, v104
	v_mov_b32_dpp v102, v84 row_shr:1 row_mask:0xf bank_mask:0xf
	v_mov_b32_dpp v103, v85 row_shr:1 row_mask:0xf bank_mask:0xf
	v_mov_b32_e32 v104, v99
	v_mov_b32_dpp v144, v112 row_shr:2 row_mask:0xf bank_mask:0xf
	v_mov_b32_dpp v145, v113 row_shr:2 row_mask:0xf bank_mask:0xf
	v_mov_b32_e32 v96, v108
	v_mov_b32_e32 v97, v122
	v_mov_b32_e32 v98, v82
	v_mov_b32_e32 v99, v76
	v_pk_fma_f32 v[80:81], v[116:117], v[102:103], v[80:81]
	v_pk_fma_f32 v[102:103], v[96:97], v[144:145], v[98:99]
	v_cvt_f32_i32_e32 v145, v13
	v_cvt_f32_i32_e32 v144, v37
	s_nop 0
	s_nop 0
	v_pk_fma_f32 v[80:81], v[84:85], v[104:105], v[80:81]
	v_mov_b32_dpp v142, v114 row_ror:1 row_mask:0xf bank_mask:0xf
	s_nop 0
	v_mov_b32_dpp v146, v115 row_ror:2 row_mask:0xf bank_mask:0xf
	s_nop 0
	v_mov_b32_dpp v114, v115 row_ror:1 row_mask:0xf bank_mask:0xf
	s_nop 0
	s_nop 0
	v_mov_b32_dpp v143, v86 row_ror:1 row_mask:0xf bank_mask:0xf
	v_mov_b32_dpp v115, v87 row_ror:1 row_mask:0xf bank_mask:0xf
	v_mov_b32_dpp v147, v87 row_ror:2 row_mask:0xf bank_mask:0xf
	v_pk_mul_f32 v[86:87], v[172:173], v[144:145]
	v_mul_f32_e32 v108, 0xbfb8aa3b, v80
	v_mov_b32_e32 v122, v109
	v_mov_b32_dpp v146, v86 row_shr:2 row_mask:0xf bank_mask:0xf
	v_mov_b32_dpp v147, v87 row_shr:2 row_mask:0xf bank_mask:0xf
	v_mov_b32_e32 v76, v83
	v_exp_f32_e32 v108, v108
	v_mov_b32_dpp v142, v112 row_shr:1 row_mask:0xf bank_mask:0xf
	v_mov_b32_dpp v143, v113 row_shr:1 row_mask:0xf bank_mask:0xf
	v_mov_b32_e32 v100, v110
	v_mov_b32_e32 v101, v118
	v_mov_b32_dpp v114, v86 row_shr:1 row_mask:0xf bank_mask:0xf
	v_mov_b32_dpp v115, v87 row_shr:1 row_mask:0xf bank_mask:0xf
	v_pk_fma_f32 v[82:83], v[122:123], v[146:147], v[76:77]
	v_mov_b32_e32 v118, v111
	v_pk_fma_f32 v[142:143], v[100:101], v[142:143], v[102:103]
	v_mov_b32_e32 v102, v140
	v_mov_b32_e32 v103, v106
	v_pk_fma_f32 v[82:83], v[118:119], v[114:115], v[82:83]
	v_mov_b32_e32 v106, v141
	v_pk_fma_f32 v[142:143], v[112:113], v[102:103], v[142:143]
	v_pk_fma_f32 v[82:83], v[86:87], v[106:107], v[82:83]
	v_pk_fma_f32 v[212:213], v[210:211], v[94:95], v[212:213]
	v_add_f32_e32 v108, 1.0, v108
	v_mul_f32_e32 v109, 0xbfb8aa3b, v142
	v_mul_f32_e32 v110, 0xbfb8aa3b, v82
	v_mul_f32_e32 v79, 0xbfb8aa3b, v212
	v_rcp_f32_e32 v108, v108
	v_exp_f32_e32 v109, v109
	v_exp_f32_e32 v110, v110
	v_exp_f32_e32 v79, v79
	v_mul_f32_e32 v80, v80, v108
	v_add_f32_e32 v108, 1.0, v109
	v_add_f32_e32 v109, 1.0, v110
	v_add_f32_e32 v79, 1.0, v79
	v_rcp_f32_e32 v108, v108
	v_rcp_f32_e32 v109, v109
	v_rcp_f32_e32 v79, v79
	v_cvt_f32_i32_e32 v141, v6
	v_cvt_f32_i32_e32 v140, v30
	v_mul_f32_e32 v80, v80, v81
	v_mul_f32_e32 v81, v142, v108
	v_mul_f32_e32 v82, v82, v109
	v_mul_f32_e32 v79, v212, v79
	v_mul_f32_e32 v81, v81, v143
	v_mul_f32_e32 v82, v82, v83
	v_mov_b32_e32 v171, v170
	v_mul_f32_e32 v79, v79, v213
	v_cvt_pk_bf16_f32 v80, v79, v80
	v_cvt_pk_bf16_f32 v81, v81, v82
	s_nop 0
	s_nop 0
	global_store_dwordx2 v[124:125], v[80:81], off offset:8
	s_nop 0
	v_mov_b32_dpp v82, v210 row_ror:2 row_mask:0xf bank_mask:0xf
	s_nop 0
	v_mov_b32_dpp v83, v211 row_ror:2 row_mask:0xf bank_mask:0xf
	v_pk_mul_f32 v[140:141], v[170:171], v[140:141]
	v_mov_b32_dpp v80, v210 row_ror:1 row_mask:0xf bank_mask:0xf
	v_mov_b32_dpp v81, v211 row_ror:1 row_mask:0xf bank_mask:0xf
	v_mov_b32_dpp v82, v140 row_shr:2 row_mask:0xf bank_mask:0xf
	v_mov_b32_dpp v83, v141 row_shr:2 row_mask:0xf bank_mask:0xf
	v_mov_b32_dpp v80, v140 row_shr:1 row_mask:0xf bank_mask:0xf
	v_mov_b32_dpp v81, v141 row_shr:1 row_mask:0xf bank_mask:0xf
	v_pk_fma_f32 v[82:83], v[88:89], v[82:83], v[90:91]
	s_nop 0
	v_pk_fma_f32 v[80:81], v[92:93], v[80:81], v[82:83]
	v_cvt_f32_i32_e32 v83, v7
	v_cvt_f32_i32_e32 v82, v31
	s_nop 0
	s_nop 0
	v_mov_b32_dpp v110, v84 row_ror:2 row_mask:0xf bank_mask:0xf
	s_nop 0
	v_mov_b32_dpp v111, v85 row_ror:2 row_mask:0xf bank_mask:0xf
	v_pk_mul_f32 v[82:83], v[170:171], v[82:83]
	v_mov_b32_dpp v108, v84 row_ror:1 row_mask:0xf bank_mask:0xf
	v_mov_b32_dpp v109, v85 row_ror:1 row_mask:0xf bank_mask:0xf
	v_mov_b32_dpp v110, v82 row_shr:2 row_mask:0xf bank_mask:0xf
	v_mov_b32_dpp v111, v83 row_shr:2 row_mask:0xf bank_mask:0xf
	v_mov_b32_dpp v108, v82 row_shr:1 row_mask:0xf bank_mask:0xf
	v_mov_b32_dpp v109, v83 row_shr:1 row_mask:0xf bank_mask:0xf
	v_pk_fma_f32 v[110:111], v[120:121], v[110:111], v[74:75]
	s_nop 0
	v_pk_fma_f32 v[108:109], v[116:117], v[108:109], v[110:111]
	v_cvt_f32_i32_e32 v111, v8
	v_cvt_f32_i32_e32 v110, v32
	s_nop 0
	s_nop 0
	v_mov_b32_dpp v114, v112 row_ror:2 row_mask:0xf bank_mask:0xf
	s_nop 0
	v_mov_b32_dpp v115, v113 row_ror:2 row_mask:0xf bank_mask:0xf
	v_pk_mul_f32 v[110:111], v[170:171], v[110:111]
	v_mov_b32_dpp v84, v112 row_ror:1 row_mask:0xf bank_mask:0xf
	v_mov_b32_dpp v85, v113 row_ror:1 row_mask:0xf bank_mask:0xf
	v_mov_b32_dpp v114, v110 row_shr:2 row_mask:0xf bank_mask:0xf
	v_mov_b32_dpp v115, v111 row_shr:2 row_mask:0xf bank_mask:0xf
	v_pk_fma_f32 v[80:81], v[140:141], v[94:95], v[80:81]
	v_mov_b32_dpp v84, v110 row_shr:1 row_mask:0xf bank_mask:0xf
	v_mov_b32_dpp v85, v111 row_shr:1 row_mask:0xf bank_mask:0xf
	v_pk_fma_f32 v[114:115], v[96:97], v[114:115], v[98:99]
	v_mul_f32_e32 v79, 0xbfb8aa3b, v80
	v_pk_fma_f32 v[84:85], v[100:101], v[84:85], v[114:115]
	v_cvt_f32_i32_e32 v115, v9
	v_cvt_f32_i32_e32 v114, v33
	v_exp_f32_e32 v79, v79
	s_nop 0
	s_nop 0
	s_nop 0
	s_nop 0
	v_mov_b32_dpp v112, v86 row_ror:1 row_mask:0xf bank_mask:0xf
	v_mov_b32_dpp v124, v86 row_ror:2 row_mask:0xf bank_mask:0xf
	v_mov_b32_dpp v113, v87 row_ror:1 row_mask:0xf bank_mask:0xf
	v_mov_b32_dpp v125, v87 row_ror:2 row_mask:0xf bank_mask:0xf
	v_pk_mul_f32 v[86:87], v[170:171], v[114:115]
	v_add_f32_e32 v79, 1.0, v79
	v_pk_fma_f32 v[108:109], v[82:83], v[104:105], v[108:109]
	v_mov_b32_dpp v124, v86 row_shr:2 row_mask:0xf bank_mask:0xf
	v_mov_b32_dpp v125, v87 row_shr:2 row_mask:0xf bank_mask:0xf
	v_mov_b32_dpp v112, v86 row_shr:1 row_mask:0xf bank_mask:0xf
	v_mov_b32_dpp v113, v87 row_shr:1 row_mask:0xf bank_mask:0xf
	v_pk_fma_f32 v[114:115], v[122:123], v[124:125], v[76:77]
	v_rcp_f32_e32 v79, v79
	v_pk_fma_f32 v[112:113], v[118:119], v[112:113], v[114:115]
	v_mul_f32_e32 v114, 0xbfb8aa3b, v108
	v_exp_f32_e32 v114, v114
	v_pk_fma_f32 v[84:85], v[110:111], v[102:103], v[84:85]
	v_mul_f32_e32 v79, v80, v79
	v_pk_fma_f32 v[112:113], v[86:87], v[106:107], v[112:113]
	v_mul_f32_e32 v79, v79, v81
	v_mul_f32_e32 v81, 0xbfb8aa3b, v84
	v_add_f32_e32 v80, 1.0, v114
	v_exp_f32_e32 v81, v81
	v_mul_f32_e32 v114, 0xbfb8aa3b, v112
	v_rcp_f32_e32 v80, v80
	v_exp_f32_e32 v114, v114
	v_add_f32_e32 v81, 1.0, v81
	v_rcp_f32_e32 v81, v81
	v_mul_f32_e32 v80, v108, v80
	v_add_f32_e32 v108, 1.0, v114
	v_rcp_f32_e32 v108, v108
	v_mul_f32_e32 v81, v84, v81
	v_mul_f32_e32 v80, v80, v109
	v_mul_f32_e32 v81, v81, v85
	v_mul_f32_e32 v84, v112, v108
	v_mul_f32_e32 v84, v84, v113
	v_cvt_pk_bf16_f32 v80, v79, v80
	v_cvt_pk_bf16_f32 v81, v81, v84
	global_store_dwordx2 v[126:127], v[80:81], off offset:8
	v_cvt_f32_i32_e32 v127, v2
	v_cvt_f32_i32_e32 v126, v26
	v_mov_b32_e32 v169, v168
	s_nop 0
	s_nop 0
	s_nop 0
	v_mov_b32_dpp v84, v140 row_ror:2 row_mask:0xf bank_mask:0xf
	s_nop 0
	v_mov_b32_dpp v85, v141 row_ror:2 row_mask:0xf bank_mask:0xf
	v_pk_mul_f32 v[126:127], v[168:169], v[126:127]
	v_mov_b32_dpp v80, v140 row_ror:1 row_mask:0xf bank_mask:0xf
	v_mov_b32_dpp v81, v141 row_ror:1 row_mask:0xf bank_mask:0xf
	v_mov_b32_dpp v84, v126 row_shr:2 row_mask:0xf bank_mask:0xf
	v_mov_b32_dpp v85, v127 row_shr:2 row_mask:0xf bank_mask:0xf
	v_mov_b32_dpp v80, v126 row_shr:1 row_mask:0xf bank_mask:0xf
	v_mov_b32_dpp v81, v127 row_shr:1 row_mask:0xf bank_mask:0xf
	v_pk_fma_f32 v[84:85], v[88:89], v[84:85], v[90:91]
	s_nop 0
	v_pk_fma_f32 v[80:81], v[92:93], v[80:81], v[84:85]
	v_cvt_f32_i32_e32 v85, v3
	v_cvt_f32_i32_e32 v84, v27
	s_nop 0
	s_nop 0
	v_mov_b32_dpp v112, v82 row_ror:2 row_mask:0xf bank_mask:0xf
	s_nop 0
	v_mov_b32_dpp v113, v83 row_ror:2 row_mask:0xf bank_mask:0xf
	v_pk_mul_f32 v[84:85], v[168:169], v[84:85]
	v_mov_b32_dpp v108, v82 row_ror:1 row_mask:0xf bank_mask:0xf
	v_mov_b32_dpp v109, v83 row_ror:1 row_mask:0xf bank_mask:0xf
	v_mov_b32_dpp v112, v84 row_shr:2 row_mask:0xf bank_mask:0xf
	v_mov_b32_dpp v113, v85 row_shr:2 row_mask:0xf bank_mask:0xf
	v_mov_b32_dpp v108, v84 row_shr:1 row_mask:0xf bank_mask:0xf
	v_mov_b32_dpp v109, v85 row_shr:1 row_mask:0xf bank_mask:0xf
	v_pk_fma_f32 v[112:113], v[120:121], v[112:113], v[74:75]
	s_nop 0
	v_pk_fma_f32 v[108:109], v[116:117], v[108:109], v[112:113]
	v_cvt_f32_i32_e32 v113, v4
	v_cvt_f32_i32_e32 v112, v28
	s_nop 0
	s_nop 0
	v_mov_b32_dpp v114, v110 row_ror:2 row_mask:0xf bank_mask:0xf
	s_nop 0
	v_mov_b32_dpp v115, v111 row_ror:2 row_mask:0xf bank_mask:0xf
	v_pk_mul_f32 v[112:113], v[168:169], v[112:113]
	v_mov_b32_dpp v82, v110 row_ror:1 row_mask:0xf bank_mask:0xf
	v_mov_b32_dpp v83, v111 row_ror:1 row_mask:0xf bank_mask:0xf
	v_mov_b32_dpp v114, v112 row_shr:2 row_mask:0xf bank_mask:0xf
	v_mov_b32_dpp v115, v113 row_shr:2 row_mask:0xf bank_mask:0xf
	v_pk_fma_f32 v[80:81], v[126:127], v[94:95], v[80:81]
	v_mov_b32_dpp v82, v112 row_shr:1 row_mask:0xf bank_mask:0xf
	v_mov_b32_dpp v83, v113 row_shr:1 row_mask:0xf bank_mask:0xf
	v_pk_fma_f32 v[114:115], v[96:97], v[114:115], v[98:99]
	v_mul_f32_e32 v79, 0xbfb8aa3b, v80
	v_pk_fma_f32 v[82:83], v[100:101], v[82:83], v[114:115]
	v_cvt_f32_i32_e32 v115, v5
	v_cvt_f32_i32_e32 v114, v29
	v_exp_f32_e32 v79, v79
	s_nop 0
	s_nop 0
	s_nop 0
	s_nop 0
	v_mov_b32_dpp v110, v86 row_ror:1 row_mask:0xf bank_mask:0xf
	v_mov_b32_dpp v124, v86 row_ror:2 row_mask:0xf bank_mask:0xf
	v_mov_b32_dpp v111, v87 row_ror:1 row_mask:0xf bank_mask:0xf
	v_mov_b32_dpp v125, v87 row_ror:2 row_mask:0xf bank_mask:0xf
	v_pk_mul_f32 v[86:87], v[168:169], v[114:115]
	v_add_f32_e32 v79, 1.0, v79
	v_pk_fma_f32 v[108:109], v[84:85], v[104:105], v[108:109]
	v_mov_b32_dpp v124, v86 row_shr:2 row_mask:0xf bank_mask:0xf
	v_mov_b32_dpp v125, v87 row_shr:2 row_mask:0xf bank_mask:0xf
	v_mov_b32_dpp v110, v86 row_shr:1 row_mask:0xf bank_mask:0xf
	v_mov_b32_dpp v111, v87 row_shr:1 row_mask:0xf bank_mask:0xf
	v_pk_fma_f32 v[114:115], v[122:123], v[124:125], v[76:77]
	v_rcp_f32_e32 v79, v79
	v_pk_fma_f32 v[110:111], v[118:119], v[110:111], v[114:115]
	v_mul_f32_e32 v114, 0xbfb8aa3b, v108
	v_exp_f32_e32 v114, v114
	v_pk_fma_f32 v[82:83], v[112:113], v[102:103], v[82:83]
	v_mul_f32_e32 v79, v80, v79
	v_pk_fma_f32 v[110:111], v[86:87], v[106:107], v[110:111]
	v_mul_f32_e32 v79, v79, v81
	v_mul_f32_e32 v81, 0xbfb8aa3b, v82
	v_add_f32_e32 v80, 1.0, v114
	v_exp_f32_e32 v81, v81
	v_mul_f32_e32 v114, 0xbfb8aa3b, v110
	v_rcp_f32_e32 v80, v80
	v_exp_f32_e32 v114, v114
	v_add_f32_e32 v81, 1.0, v81
	v_rcp_f32_e32 v81, v81
	v_mul_f32_e32 v80, v108, v80
	v_add_f32_e32 v108, 1.0, v114
	v_rcp_f32_e32 v108, v108
	v_mul_f32_e32 v81, v82, v81
	v_mul_f32_e32 v80, v80, v109
	v_mul_f32_e32 v81, v81, v83
	v_mul_f32_e32 v82, v110, v108
	v_mul_f32_e32 v82, v82, v111
	v_cvt_pk_bf16_f32 v80, v79, v80
	v_cvt_pk_bf16_f32 v81, v81, v82
	v_mov_b32_e32 v175, v174
	global_store_dwordx2 v[128:129], v[80:81], off offset:8
	s_nop 0
	s_nop 0
	s_nop 0
	s_nop 0
	v_mov_b32_dpp v80, v126 row_ror:1 row_mask:0xf bank_mask:0xf
	v_mov_b32_dpp v82, v126 row_ror:2 row_mask:0xf bank_mask:0xf
	v_mov_b32_dpp v81, v127 row_ror:1 row_mask:0xf bank_mask:0xf
	v_mov_b32_dpp v83, v127 row_ror:2 row_mask:0xf bank_mask:0xf
	v_pk_mul_f32 v[126:127], v[174:175], v[182:183]
	s_nop 0
	s_nop 0
	v_mov_b32_dpp v82, v126 row_shr:2 row_mask:0xf bank_mask:0xf
	v_mov_b32_dpp v83, v127 row_shr:2 row_mask:0xf bank_mask:0xf
	v_mov_b32_dpp v80, v126 row_shr:1 row_mask:0xf bank_mask:0xf
	v_mov_b32_dpp v81, v127 row_shr:1 row_mask:0xf bank_mask:0xf
	v_pk_fma_f32 v[82:83], v[88:89], v[82:83], v[90:91]
	s_nop 0
	v_pk_fma_f32 v[80:81], v[92:93], v[80:81], v[82:83]
	v_mov_b32_dpp v110, v84 row_ror:2 row_mask:0xf bank_mask:0xf
	v_pk_fma_f32 v[80:81], v[126:127], v[94:95], v[80:81]
	s_nop 0
	v_mov_b32_dpp v111, v85 row_ror:2 row_mask:0xf bank_mask:0xf
	v_pk_mul_f32 v[82:83], v[174:175], v[178:179]
	v_mov_b32_dpp v108, v84 row_ror:1 row_mask:0xf bank_mask:0xf
	v_mov_b32_dpp v109, v85 row_ror:1 row_mask:0xf bank_mask:0xf
	v_mov_b32_dpp v110, v82 row_shr:2 row_mask:0xf bank_mask:0xf
	v_mov_b32_dpp v111, v83 row_shr:2 row_mask:0xf bank_mask:0xf
	v_mul_f32_e32 v79, 0xbfb8aa3b, v80
	v_mov_b32_dpp v108, v82 row_shr:1 row_mask:0xf bank_mask:0xf
	v_mov_b32_dpp v109, v83 row_shr:1 row_mask:0xf bank_mask:0xf
	v_pk_fma_f32 v[110:111], v[120:121], v[110:111], v[74:75]
	v_exp_f32_e32 v79, v79
	s_nop 0
	v_pk_fma_f32 v[108:109], v[116:117], v[108:109], v[110:111]
	s_nop 0
	s_nop 0
	v_mov_b32_dpp v114, v112 row_ror:2 row_mask:0xf bank_mask:0xf
	v_pk_fma_f32 v[82:83], v[82:83], v[104:105], v[108:109]
	s_nop 0
	v_mov_b32_dpp v115, v113 row_ror:2 row_mask:0xf bank_mask:0xf
	v_pk_mul_f32 v[108:109], v[174:175], v[180:181]
	v_mov_b32_dpp v84, v112 row_ror:1 row_mask:0xf bank_mask:0xf
	v_mov_b32_dpp v85, v113 row_ror:1 row_mask:0xf bank_mask:0xf
	v_mov_b32_dpp v114, v108 row_shr:2 row_mask:0xf bank_mask:0xf
	v_mov_b32_dpp v115, v109 row_shr:2 row_mask:0xf bank_mask:0xf
	s_nop 0
	s_nop 0
	v_mov_b32_dpp v84, v108 row_shr:1 row_mask:0xf bank_mask:0xf
	v_mov_b32_dpp v85, v109 row_shr:1 row_mask:0xf bank_mask:0xf
	v_pk_fma_f32 v[110:111], v[96:97], v[114:115], v[98:99]
	s_nop 0
	s_nop 0
	v_add_f32_e32 v79, 1.0, v79
	v_mov_b32_dpp v112, v86 row_ror:1 row_mask:0xf bank_mask:0xf
	v_mov_b32_dpp v124, v86 row_ror:2 row_mask:0xf bank_mask:0xf
	v_pk_fma_f32 v[84:85], v[100:101], v[84:85], v[110:111]
	v_mov_b32_dpp v113, v87 row_ror:1 row_mask:0xf bank_mask:0xf
	v_mov_b32_dpp v125, v87 row_ror:2 row_mask:0xf bank_mask:0xf
	v_pk_mul_f32 v[86:87], v[174:175], v[176:177]
	v_rcp_f32_e32 v79, v79
	v_mul_f32_e32 v110, 0xbfb8aa3b, v82
	v_mov_b32_dpp v124, v86 row_shr:2 row_mask:0xf bank_mask:0xf
	v_mov_b32_dpp v125, v87 row_shr:2 row_mask:0xf bank_mask:0xf
	v_exp_f32_e32 v110, v110
	v_pk_fma_f32 v[84:85], v[108:109], v[102:103], v[84:85]
	v_mov_b32_dpp v112, v86 row_shr:1 row_mask:0xf bank_mask:0xf
	v_mov_b32_dpp v113, v87 row_shr:1 row_mask:0xf bank_mask:0xf
	v_pk_fma_f32 v[108:109], v[122:123], v[124:125], v[76:77]
	v_mul_f32_e32 v79, v80, v79
	v_pk_fma_f32 v[108:109], v[118:119], v[112:113], v[108:109]
	v_mul_f32_e32 v79, v79, v81
	v_pk_fma_f32 v[86:87], v[86:87], v[106:107], v[108:109]
	v_add_f32_e32 v80, 1.0, v110
	v_mul_f32_e32 v81, 0xbfb8aa3b, v84
	v_mul_f32_e32 v108, 0xbfb8aa3b, v86
	v_rcp_f32_e32 v80, v80
	v_exp_f32_e32 v81, v81
	v_exp_f32_e32 v108, v108
	v_mov_b32_e32 v78, 0
	v_mul_f32_e32 v80, v82, v80
	v_add_f32_e32 v81, 1.0, v81
	v_add_f32_e32 v82, 1.0, v108
	v_rcp_f32_e32 v81, v81
	v_rcp_f32_e32 v82, v82
	v_mul_f32_e32 v80, v80, v83
	v_cvt_pk_bf16_f32 v80, v79, v80
	v_mul_f32_e32 v81, v84, v81
	v_mul_f32_e32 v82, v86, v82
	v_mul_f32_e32 v81, v81, v85
	v_mul_f32_e32 v82, v82, v87
	v_cvt_pk_bf16_f32 v81, v81, v82
	v_mov_b32_e32 v82, 0
	v_mov_b32_e32 v83, 0
	v_mov_b32_e32 v84, 0
	v_mov_b32_e32 v85, 0
	global_store_dwordx2 v[132:133], v[80:81], off offset:8
	s_and_saveexec_b64 s[0:1], vcc
	ds_read_b128 v[82:85], v195 offset:16
	s_or_b64 exec, exec, s[0:1]
	v_mov_b32_e32 v79, 0
	v_mov_b32_e32 v80, 0
	v_mov_b32_e32 v81, 0
	s_and_saveexec_b64 s[0:1], vcc
	ds_read_b128 v[78:81], v195 offset:528
	s_or_b64 exec, exec, s[0:1]
	v_cvt_f32_i32_e32 v127, v66
	v_cvt_f32_i32_e32 v67, v67
	v_cvt_f32_i32_e32 v66, v71
	v_cvt_f32_i32_e32 v126, v70
	s_nop 0
	s_nop 0
	v_mov_b32_e32 v209, v208
	s_waitcnt lgkmcnt(0)
	v_mov_b32_dpp v86, v82 row_ror:1 row_mask:0xf bank_mask:0xf
	v_mov_b32_dpp v108, v82 row_ror:2 row_mask:0xf bank_mask:0xf
	s_nop 0
	s_nop 0
	s_nop 0
	v_mov_b32_dpp v82, v83 row_ror:1 row_mask:0xf bank_mask:0xf
	v_mov_b32_dpp v110, v83 row_ror:2 row_mask:0xf bank_mask:0xf
	s_nop 0
	s_nop 0
	s_nop 0
	v_mov_b32_dpp v111, v79 row_ror:2 row_mask:0xf bank_mask:0xf
	v_pk_mul_f32 v[66:67], v[208:209], v[66:67]
	v_mov_b32_dpp v87, v78 row_ror:1 row_mask:0xf bank_mask:0xf
	v_mov_b32_dpp v109, v78 row_ror:2 row_mask:0xf bank_mask:0xf
	v_pk_mul_f32 v[126:127], v[208:209], v[126:127]
	v_mov_b32_dpp v83, v79 row_ror:1 row_mask:0xf bank_mask:0xf
	v_mov_b32_dpp v110, v66 row_shr:2 row_mask:0xf bank_mask:0xf
	v_mov_b32_dpp v111, v67 row_shr:2 row_mask:0xf bank_mask:0xf
	v_cvt_f32_i32_e32 v79, v68
	v_cvt_f32_i32_e32 v78, v72
	v_cvt_f32_i32_e32 v69, v69
	v_cvt_f32_i32_e32 v68, v73
	s_nop 0
	s_nop 0
	v_mov_b32_dpp v108, v126 row_shr:2 row_mask:0xf bank_mask:0xf
	v_mov_b32_dpp v109, v127 row_shr:2 row_mask:0xf bank_mask:0xf
	v_mov_b32_dpp v82, v66 row_shr:1 row_mask:0xf bank_mask:0xf
	v_mov_b32_dpp v83, v67 row_shr:1 row_mask:0xf bank_mask:0xf
	v_pk_fma_f32 v[70:71], v[120:121], v[110:111], v[74:75]
	v_mov_b32_dpp v112, v84 row_ror:1 row_mask:0xf bank_mask:0xf
	v_mov_b32_dpp v114, v84 row_ror:2 row_mask:0xf bank_mask:0xf
	s_nop 0
	s_nop 0
	v_mov_b32_dpp v86, v126 row_shr:1 row_mask:0xf bank_mask:0xf
	v_mov_b32_dpp v87, v127 row_shr:1 row_mask:0xf bank_mask:0xf
	v_pk_fma_f32 v[108:109], v[88:89], v[108:109], v[90:91]
	v_pk_fma_f32 v[70:71], v[116:117], v[82:83], v[70:71]
	v_mov_b32_dpp v84, v85 row_ror:1 row_mask:0xf bank_mask:0xf
	v_mov_b32_dpp v124, v85 row_ror:2 row_mask:0xf bank_mask:0xf
	v_pk_fma_f32 v[86:87], v[92:93], v[86:87], v[108:109]
	v_pk_fma_f32 v[70:71], v[66:67], v[104:105], v[70:71]
	s_nop 0
	s_nop 0
	s_nop 0
	v_pk_fma_f32 v[86:87], v[126:127], v[94:95], v[86:87]
	s_nop 0
	v_mov_b32_dpp v115, v80 row_ror:2 row_mask:0xf bank_mask:0xf
	v_pk_mul_f32 v[78:79], v[208:209], v[78:79]
	v_mov_b32_dpp v85, v81 row_ror:1 row_mask:0xf bank_mask:0xf
	v_mov_b32_dpp v125, v81 row_ror:2 row_mask:0xf bank_mask:0xf
	v_pk_mul_f32 v[68:69], v[208:209], v[68:69]
	v_mul_f32_e32 v81, 0xbfb8aa3b, v70
	v_mov_b32_dpp v113, v80 row_ror:1 row_mask:0xf bank_mask:0xf
	v_mov_b32_dpp v114, v78 row_shr:2 row_mask:0xf bank_mask:0xf
	v_mov_b32_dpp v115, v79 row_shr:2 row_mask:0xf bank_mask:0xf
	v_mov_b32_dpp v124, v68 row_shr:2 row_mask:0xf bank_mask:0xf
	v_mul_f32_e32 v72, 0xbfb8aa3b, v86
	v_mov_b32_dpp v125, v69 row_shr:2 row_mask:0xf bank_mask:0xf
	v_exp_f32_e32 v81, v81
	v_mov_b32_dpp v112, v78 row_shr:1 row_mask:0xf bank_mask:0xf
	v_mov_b32_dpp v113, v79 row_shr:1 row_mask:0xf bank_mask:0xf
	v_pk_fma_f32 v[82:83], v[96:97], v[114:115], v[98:99]
	v_mov_b32_dpp v84, v68 row_shr:1 row_mask:0xf bank_mask:0xf
	v_mov_b32_dpp v85, v69 row_shr:1 row_mask:0xf bank_mask:0xf
	v_exp_f32_e32 v80, v72
	v_pk_fma_f32 v[72:73], v[122:123], v[124:125], v[76:77]
	v_pk_fma_f32 v[82:83], v[100:101], v[112:113], v[82:83]
	v_pk_fma_f32 v[72:73], v[118:119], v[84:85], v[72:73]
	v_pk_fma_f32 v[82:83], v[78:79], v[102:103], v[82:83]
	v_pk_fma_f32 v[72:73], v[68:69], v[106:107], v[72:73]
	v_add_f32_e32 v81, 1.0, v81
	v_mul_f32_e32 v84, 0xbfb8aa3b, v82
	v_mul_f32_e32 v85, 0xbfb8aa3b, v72
	v_rcp_f32_e32 v81, v81
	v_exp_f32_e32 v84, v84
	v_exp_f32_e32 v85, v85
	v_add_f32_e32 v80, 1.0, v80
	v_mul_f32_e32 v70, v70, v81
	v_add_f32_e32 v81, 1.0, v84
	v_add_f32_e32 v84, 1.0, v85
	v_rcp_f32_e32 v81, v81
	v_rcp_f32_e32 v84, v84
	v_rcp_f32_e32 v80, v80
	v_cvt_f32_i32_e32 v109, v58
	v_cvt_f32_i32_e32 v108, v62
	v_mul_f32_e32 v70, v70, v71
	v_mul_f32_e32 v71, v82, v81
	v_mul_f32_e32 v72, v72, v84
	v_mul_f32_e32 v80, v86, v80
	v_mul_f32_e32 v71, v71, v83
	v_mul_f32_e32 v72, v72, v73
	v_mov_b32_e32 v207, v206
	v_mul_f32_e32 v80, v80, v87
	v_cvt_pk_bf16_f32 v70, v80, v70
	v_cvt_pk_bf16_f32 v71, v71, v72
	s_nop 0
	s_nop 0
	global_store_dwordx2 v[130:131], v[70:71], off offset:8
	s_nop 0
	v_mov_b32_dpp v72, v126 row_ror:2 row_mask:0xf bank_mask:0xf
	s_nop 0
	v_mov_b32_dpp v73, v127 row_ror:2 row_mask:0xf bank_mask:0xf
	v_pk_mul_f32 v[108:109], v[206:207], v[108:109]
	v_mov_b32_dpp v70, v126 row_ror:1 row_mask:0xf bank_mask:0xf
	v_mov_b32_dpp v71, v127 row_ror:1 row_mask:0xf bank_mask:0xf
	v_mov_b32_dpp v72, v108 row_shr:2 row_mask:0xf bank_mask:0xf
	v_mov_b32_dpp v73, v109 row_shr:2 row_mask:0xf bank_mask:0xf
	v_mov_b32_dpp v70, v108 row_shr:1 row_mask:0xf bank_mask:0xf
	v_mov_b32_dpp v71, v109 row_shr:1 row_mask:0xf bank_mask:0xf
	v_pk_fma_f32 v[72:73], v[88:89], v[72:73], v[90:91]
	v_cvt_f32_i32_e32 v59, v59
	v_cvt_f32_i32_e32 v58, v63
	s_nop 0
	s_nop 0
	v_pk_fma_f32 v[70:71], v[92:93], v[70:71], v[72:73]
	v_mov_b32_dpp v80, v66 row_ror:1 row_mask:0xf bank_mask:0xf
	v_mov_b32_dpp v82, v66 row_ror:2 row_mask:0xf bank_mask:0xf
	s_nop 0
	s_nop 0
	v_pk_fma_f32 v[70:71], v[108:109], v[94:95], v[70:71]
	v_mov_b32_dpp v66, v78 row_ror:1 row_mask:0xf bank_mask:0xf
	v_mov_b32_dpp v84, v78 row_ror:2 row_mask:0xf bank_mask:0xf
	s_nop 0
	s_nop 0
	s_nop 0
	v_cvt_f32_i32_e32 v72, v64
	v_mul_f32_e32 v64, 0xbfb8aa3b, v70
	v_mov_b32_dpp v78, v68 row_ror:1 row_mask:0xf bank_mask:0xf
	v_mov_b32_dpp v86, v68 row_ror:2 row_mask:0xf bank_mask:0xf
	s_nop 0
	v_mov_b32_dpp v83, v67 row_ror:2 row_mask:0xf bank_mask:0xf
	v_pk_mul_f32 v[58:59], v[206:207], v[58:59]
	v_exp_f32_e32 v68, v64
	v_mov_b32_dpp v81, v67 row_ror:1 row_mask:0xf bank_mask:0xf
	v_mov_b32_dpp v82, v58 row_shr:2 row_mask:0xf bank_mask:0xf
	v_mov_b32_dpp v83, v59 row_shr:2 row_mask:0xf bank_mask:0xf
	v_cvt_f32_i32_e32 v73, v60
	v_cvt_f32_i32_e32 v61, v61
	v_cvt_f32_i32_e32 v60, v65
	v_mov_b32_dpp v80, v58 row_shr:1 row_mask:0xf bank_mask:0xf
	v_mov_b32_dpp v81, v59 row_shr:1 row_mask:0xf bank_mask:0xf
	v_pk_fma_f32 v[62:63], v[120:121], v[82:83], v[74:75]
	s_nop 0
	v_pk_fma_f32 v[62:63], v[116:117], v[80:81], v[62:63]
	s_nop 0
	v_pk_fma_f32 v[62:63], v[58:59], v[104:105], v[62:63]
	v_mov_b32_dpp v67, v79 row_ror:1 row_mask:0xf bank_mask:0xf
	v_mov_b32_dpp v85, v79 row_ror:2 row_mask:0xf bank_mask:0xf
	s_nop 0
	s_nop 0
	v_add_f32_e32 v68, 1.0, v68
	v_pk_mul_f32 v[72:73], v[206:207], v[72:73]
	v_mov_b32_dpp v79, v69 row_ror:1 row_mask:0xf bank_mask:0xf
	v_mov_b32_dpp v87, v69 row_ror:2 row_mask:0xf bank_mask:0xf
	v_pk_mul_f32 v[60:61], v[206:207], v[60:61]
	v_rcp_f32_e32 v68, v68
	v_mul_f32_e32 v69, 0xbfb8aa3b, v62
	v_mov_b32_dpp v84, v72 row_shr:2 row_mask:0xf bank_mask:0xf
	v_mov_b32_dpp v85, v73 row_shr:2 row_mask:0xf bank_mask:0xf
	v_mov_b32_dpp v86, v60 row_shr:2 row_mask:0xf bank_mask:0xf
	v_mov_b32_dpp v87, v61 row_shr:2 row_mask:0xf bank_mask:0xf
	v_exp_f32_e32 v69, v69
	v_mov_b32_dpp v66, v72 row_shr:1 row_mask:0xf bank_mask:0xf
	v_mov_b32_dpp v67, v73 row_shr:1 row_mask:0xf bank_mask:0xf
	v_pk_fma_f32 v[80:81], v[96:97], v[84:85], v[98:99]
	v_mov_b32_dpp v78, v60 row_shr:1 row_mask:0xf bank_mask:0xf
	v_mov_b32_dpp v79, v61 row_shr:1 row_mask:0xf bank_mask:0xf
	v_pk_fma_f32 v[64:65], v[122:123], v[86:87], v[76:77]
	v_pk_fma_f32 v[66:67], v[100:101], v[66:67], v[80:81]
	v_pk_fma_f32 v[64:65], v[118:119], v[78:79], v[64:65]
	v_pk_fma_f32 v[66:67], v[72:73], v[102:103], v[66:67]
	v_pk_fma_f32 v[64:65], v[60:61], v[106:107], v[64:65]
	v_mul_f32_e32 v68, v70, v68
	v_mul_f32_e32 v68, v68, v71
	v_add_f32_e32 v69, 1.0, v69
	v_mul_f32_e32 v70, 0xbfb8aa3b, v66
	v_mul_f32_e32 v71, 0xbfb8aa3b, v64
	v_rcp_f32_e32 v69, v69
	v_exp_f32_e32 v70, v70
	v_exp_f32_e32 v71, v71
	v_cvt_f32_i32_e32 v81, v50
	v_mul_f32_e32 v62, v62, v69
	v_add_f32_e32 v69, 1.0, v70
	v_add_f32_e32 v70, 1.0, v71
	v_rcp_f32_e32 v69, v69
	v_rcp_f32_e32 v70, v70
	v_cvt_f32_i32_e32 v80, v54
	v_mul_f32_e32 v62, v62, v63
	v_mul_f32_e32 v63, v66, v69
	v_mul_f32_e32 v64, v64, v70
	v_mul_f32_e32 v63, v63, v67
	v_mul_f32_e32 v64, v64, v65
	v_mov_b32_e32 v199, v198
	v_cvt_pk_bf16_f32 v62, v68, v62
	v_cvt_pk_bf16_f32 v63, v63, v64
	s_nop 0
	s_nop 0
	global_store_dwordx2 v[134:135], v[62:63], off offset:8
	s_nop 0
	v_mov_b32_dpp v64, v108 row_ror:2 row_mask:0xf bank_mask:0xf
	s_nop 0
	v_mov_b32_dpp v65, v109 row_ror:2 row_mask:0xf bank_mask:0xf
	v_pk_mul_f32 v[80:81], v[198:199], v[80:81]
	v_mov_b32_dpp v62, v108 row_ror:1 row_mask:0xf bank_mask:0xf
	v_mov_b32_dpp v63, v109 row_ror:1 row_mask:0xf bank_mask:0xf
	v_mov_b32_dpp v64, v80 row_shr:2 row_mask:0xf bank_mask:0xf
	v_mov_b32_dpp v65, v81 row_shr:2 row_mask:0xf bank_mask:0xf
	v_mov_b32_dpp v62, v80 row_shr:1 row_mask:0xf bank_mask:0xf
	v_mov_b32_dpp v63, v81 row_shr:1 row_mask:0xf bank_mask:0xf
	v_pk_fma_f32 v[64:65], v[88:89], v[64:65], v[90:91]
	v_cvt_f32_i32_e32 v51, v51
	v_cvt_f32_i32_e32 v50, v55
	s_nop 0
	s_nop 0
	v_pk_fma_f32 v[62:63], v[92:93], v[62:63], v[64:65]
	v_mov_b32_dpp v66, v58 row_ror:1 row_mask:0xf bank_mask:0xf
	v_mov_b32_dpp v68, v58 row_ror:2 row_mask:0xf bank_mask:0xf
	s_nop 0
	s_nop 0
	v_pk_fma_f32 v[62:63], v[80:81], v[94:95], v[62:63]
	v_mov_b32_dpp v58, v72 row_ror:1 row_mask:0xf bank_mask:0xf
	v_mov_b32_dpp v70, v72 row_ror:2 row_mask:0xf bank_mask:0xf
	s_nop 0
	s_nop 0
	s_nop 0
	v_cvt_f32_i32_e32 v64, v56
	v_mul_f32_e32 v56, 0xbfb8aa3b, v62
	v_mov_b32_dpp v72, v60 row_ror:1 row_mask:0xf bank_mask:0xf
	v_mov_b32_dpp v78, v60 row_ror:2 row_mask:0xf bank_mask:0xf
	s_nop 0
	v_mov_b32_dpp v69, v59 row_ror:2 row_mask:0xf bank_mask:0xf
	v_pk_mul_f32 v[50:51], v[198:199], v[50:51]
	v_exp_f32_e32 v60, v56
	v_mov_b32_dpp v67, v59 row_ror:1 row_mask:0xf bank_mask:0xf
	v_mov_b32_dpp v68, v50 row_shr:2 row_mask:0xf bank_mask:0xf
	v_mov_b32_dpp v69, v51 row_shr:2 row_mask:0xf bank_mask:0xf
	v_cvt_f32_i32_e32 v65, v52
	v_cvt_f32_i32_e32 v53, v53
	v_cvt_f32_i32_e32 v52, v57
	v_mov_b32_dpp v66, v50 row_shr:1 row_mask:0xf bank_mask:0xf
	v_mov_b32_dpp v67, v51 row_shr:1 row_mask:0xf bank_mask:0xf
	v_pk_fma_f32 v[54:55], v[120:121], v[68:69], v[74:75]
	s_nop 0
	v_pk_fma_f32 v[54:55], v[116:117], v[66:67], v[54:55]
	s_nop 0
	v_pk_fma_f32 v[54:55], v[50:51], v[104:105], v[54:55]
	v_mov_b32_dpp v59, v73 row_ror:1 row_mask:0xf bank_mask:0xf
	v_mov_b32_dpp v71, v73 row_ror:2 row_mask:0xf bank_mask:0xf
	s_nop 0
	s_nop 0
	v_add_f32_e32 v60, 1.0, v60
	v_pk_mul_f32 v[64:65], v[198:199], v[64:65]
	v_mov_b32_dpp v73, v61 row_ror:1 row_mask:0xf bank_mask:0xf
	v_mov_b32_dpp v79, v61 row_ror:2 row_mask:0xf bank_mask:0xf
	v_pk_mul_f32 v[52:53], v[198:199], v[52:53]
	v_rcp_f32_e32 v60, v60
	v_mul_f32_e32 v61, 0xbfb8aa3b, v54
	v_mov_b32_dpp v70, v64 row_shr:2 row_mask:0xf bank_mask:0xf
	v_mov_b32_dpp v71, v65 row_shr:2 row_mask:0xf bank_mask:0xf
	v_mov_b32_dpp v78, v52 row_shr:2 row_mask:0xf bank_mask:0xf
	v_mov_b32_dpp v79, v53 row_shr:2 row_mask:0xf bank_mask:0xf
	v_exp_f32_e32 v61, v61
	v_mov_b32_dpp v58, v64 row_shr:1 row_mask:0xf bank_mask:0xf
	v_mov_b32_dpp v59, v65 row_shr:1 row_mask:0xf bank_mask:0xf
	v_pk_fma_f32 v[66:67], v[96:97], v[70:71], v[98:99]
	v_mov_b32_dpp v72, v52 row_shr:1 row_mask:0xf bank_mask:0xf
	v_mov_b32_dpp v73, v53 row_shr:1 row_mask:0xf bank_mask:0xf
	v_pk_fma_f32 v[56:57], v[122:123], v[78:79], v[76:77]
	v_pk_fma_f32 v[58:59], v[100:101], v[58:59], v[66:67]
	v_pk_fma_f32 v[56:57], v[118:119], v[72:73], v[56:57]
	v_pk_fma_f32 v[58:59], v[64:65], v[102:103], v[58:59]
	v_pk_fma_f32 v[56:57], v[52:53], v[106:107], v[56:57]
	v_mul_f32_e32 v60, v62, v60
	v_mul_f32_e32 v60, v60, v63
	v_add_f32_e32 v61, 1.0, v61
	v_mul_f32_e32 v62, 0xbfb8aa3b, v58
	v_mul_f32_e32 v63, 0xbfb8aa3b, v56
	v_rcp_f32_e32 v61, v61
	v_exp_f32_e32 v62, v62
	v_exp_f32_e32 v63, v63
	v_mov_b32_e32 v195, v194
	v_mul_f32_e32 v54, v54, v61
	v_add_f32_e32 v61, 1.0, v62
	v_add_f32_e32 v62, 1.0, v63
	v_rcp_f32_e32 v61, v61
	v_rcp_f32_e32 v62, v62
	v_mul_f32_e32 v54, v54, v55
	v_cvt_pk_bf16_f32 v54, v60, v54
	v_mul_f32_e32 v55, v58, v61
	v_mul_f32_e32 v56, v56, v62
	v_mul_f32_e32 v55, v55, v59
	v_mul_f32_e32 v56, v56, v57
	v_cvt_pk_bf16_f32 v55, v55, v56
	s_nop 0
	s_nop 0
	global_store_dwordx2 v[136:137], v[54:55], off offset:8
	s_nop 0
	v_mov_b32_dpp v56, v80 row_ror:2 row_mask:0xf bank_mask:0xf
	s_nop 0
	v_mov_b32_dpp v57, v81 row_ror:2 row_mask:0xf bank_mask:0xf
	v_pk_mul_f32 v[68:69], v[194:195], v[204:205]
	v_mov_b32_dpp v54, v80 row_ror:1 row_mask:0xf bank_mask:0xf
	v_mov_b32_dpp v55, v81 row_ror:1 row_mask:0xf bank_mask:0xf
	v_mov_b32_dpp v56, v68 row_shr:2 row_mask:0xf bank_mask:0xf
	v_mov_b32_dpp v57, v69 row_shr:2 row_mask:0xf bank_mask:0xf
	s_nop 0
	v_mov_b32_dpp v54, v68 row_shr:1 row_mask:0xf bank_mask:0xf
	v_mov_b32_dpp v55, v69 row_shr:1 row_mask:0xf bank_mask:0xf
	v_pk_fma_f32 v[56:57], v[88:89], v[56:57], v[90:91]
	s_nop 0
	s_nop 0
	v_mov_b32_dpp v60, v50 row_ror:2 row_mask:0xf bank_mask:0xf
	v_pk_fma_f32 v[54:55], v[92:93], v[54:55], v[56:57]
	s_nop 0
	v_mov_b32_dpp v61, v51 row_ror:2 row_mask:0xf bank_mask:0xf
	v_pk_mul_f32 v[56:57], v[194:195], v[202:203]
	v_mov_b32_dpp v58, v50 row_ror:1 row_mask:0xf bank_mask:0xf
	v_mov_b32_dpp v59, v51 row_ror:1 row_mask:0xf bank_mask:0xf
	v_mov_b32_dpp v60, v56 row_shr:2 row_mask:0xf bank_mask:0xf
	v_mov_b32_dpp v61, v57 row_shr:2 row_mask:0xf bank_mask:0xf
	v_mov_b32_dpp v58, v56 row_shr:1 row_mask:0xf bank_mask:0xf
	v_mov_b32_dpp v59, v57 row_shr:1 row_mask:0xf bank_mask:0xf
	v_pk_fma_f32 v[60:61], v[120:121], v[60:61], v[74:75]
	s_nop 0
	v_pk_fma_f32 v[58:59], v[116:117], v[58:59], v[60:61]
	s_nop 0
	s_nop 0
	v_mov_b32_dpp v62, v64 row_ror:2 row_mask:0xf bank_mask:0xf
	v_pk_fma_f32 v[56:57], v[56:57], v[104:105], v[58:59]
	s_nop 0
	v_mov_b32_dpp v63, v65 row_ror:2 row_mask:0xf bank_mask:0xf
	v_pk_mul_f32 v[58:59], v[194:195], v[200:201]
	v_mov_b32_dpp v50, v64 row_ror:1 row_mask:0xf bank_mask:0xf
	v_mov_b32_dpp v51, v65 row_ror:1 row_mask:0xf bank_mask:0xf
	v_mov_b32_dpp v62, v58 row_shr:2 row_mask:0xf bank_mask:0xf
	v_mov_b32_dpp v63, v59 row_shr:2 row_mask:0xf bank_mask:0xf
	v_mov_b32_dpp v50, v58 row_shr:1 row_mask:0xf bank_mask:0xf
	v_mov_b32_dpp v51, v59 row_shr:1 row_mask:0xf bank_mask:0xf
	v_pk_fma_f32 v[60:61], v[96:97], v[62:63], v[98:99]
	v_pk_fma_f32 v[54:55], v[68:69], v[94:95], v[54:55]
	v_pk_fma_f32 v[50:51], v[100:101], v[50:51], v[60:61]
	s_nop 0
	v_pk_fma_f32 v[50:51], v[58:59], v[102:103], v[50:51]
	v_mul_f32_e32 v58, 0xbfb8aa3b, v54
	v_exp_f32_e32 v60, v58
	s_nop 0
	s_nop 0
	s_nop 0
	v_add_f32_e32 v60, 1.0, v60
	v_rcp_f32_e32 v60, v60
	v_mul_f32_e32 v61, 0xbfb8aa3b, v56
	v_mov_b32_dpp v64, v52 row_ror:1 row_mask:0xf bank_mask:0xf
	v_mov_b32_dpp v66, v52 row_ror:2 row_mask:0xf bank_mask:0xf
	v_mov_b32_dpp v65, v53 row_ror:1 row_mask:0xf bank_mask:0xf
	v_mov_b32_dpp v67, v53 row_ror:2 row_mask:0xf bank_mask:0xf
	v_pk_mul_f32 v[52:53], v[194:195], v[196:197]
	v_exp_f32_e32 v61, v61
	v_mul_f32_e32 v54, v54, v60
	v_mov_b32_dpp v66, v52 row_shr:2 row_mask:0xf bank_mask:0xf
	v_mov_b32_dpp v67, v53 row_shr:2 row_mask:0xf bank_mask:0xf
	v_mov_b32_dpp v64, v52 row_shr:1 row_mask:0xf bank_mask:0xf
	v_mov_b32_dpp v65, v53 row_shr:1 row_mask:0xf bank_mask:0xf
	v_pk_fma_f32 v[58:59], v[122:123], v[66:67], v[76:77]
	v_mul_f32_e32 v54, v54, v55
	v_pk_fma_f32 v[58:59], v[118:119], v[64:65], v[58:59]
	v_add_f32_e32 v55, 1.0, v61
	v_pk_fma_f32 v[52:53], v[52:53], v[106:107], v[58:59]
	v_mul_f32_e32 v58, 0xbfb8aa3b, v50
	v_rcp_f32_e32 v55, v55
	v_exp_f32_e32 v58, v58
	v_mul_f32_e32 v59, 0xbfb8aa3b, v52
	v_exp_f32_e32 v59, v59
	v_mul_f32_e32 v55, v56, v55
	v_add_f32_e32 v56, 1.0, v58
	v_rcp_f32_e32 v56, v56
	v_add_f32_e32 v58, 1.0, v59
	v_rcp_f32_e32 v58, v58
	v_mul_f32_e32 v50, v50, v56
	v_mul_f32_e32 v51, v50, v51
	v_mul_f32_e32 v50, v52, v58
	v_mul_f32_e32 v55, v55, v57
	v_mul_f32_e32 v52, v50, v53
	v_cvt_pk_bf16_f32 v50, v54, v55
	v_cvt_pk_bf16_f32 v51, v51, v52
	global_store_dwordx2 v[138:139], v[50:51], off offset:8
